# w1/w3 int8 expert-weight conversion by dedicated converter WGs inside GEMM phases 2 (72 WGs, 3 rounds), 7 (54 WGs, 7 rounds), 10 (64 WGs, 6 rounds); no conversion tiles ride on HBM-bound phases 1, 6,
# speedup vs baseline: 1.0886x; 1.0339x over previous
.LBB0_168:
	global_load_dwordx4 v[94:97], v[104:105], off offset:-4096
	global_load_dwordx4 v[90:93], v[104:105], off offset:-3072
	global_load_dwordx4 v[86:89], v[104:105], off offset:-2048
	global_load_dwordx4 v[82:85], v[104:105], off offset:-1024
	global_load_dwordx4 v[78:81], v[104:105], off
	global_load_dwordx4 v[74:77], v[104:105], off offset:1024
	global_load_dwordx4 v[70:73], v[104:105], off offset:2048
	global_load_dwordx4 v[66:69], v[104:105], off offset:3072
	s_cmp_lt_i32 s75, 0
	s_cselect_b64 s[22:23], -1, 0
	s_cmp_gt_i32 s75, -1
	s_cbranch_scc1 .LBB0_173
	s_cmp_gt_i32 s75, 0xdfff
	s_mov_b64 s[2:3], -1
	s_cbranch_scc0 .LBB0_171
	s_add_i32 s2, s75, 0x2000
	s_bfe_u32 s3, s2, 0x70009
	s_mulk_i32 s3, 0x2493
	s_lshr_b32 s21, s3, 16
	s_mul_i32 s3, s21, 0xe00
	s_sub_i32 s2, s2, s3
	v_readlane_b32 s36, v250, 32
	s_and_b32 s8, s2, 0xffff
	s_mul_i32 s2, s21, 0x3800000
	v_readlane_b32 s42, v250, 38
	v_readlane_b32 s43, v250, 39
	s_add_u32 s2, s42, s2
	s_addc_u32 s3, s43, 0
	s_lshl_b32 s20, s8, 1
	s_and_b32 s20, s20, 0x1f80
	v_or_b32_e32 v2, s20, v98
	v_lshlrev_b32_e32 v102, 13, v2
	v_lshl_add_u64 v[2:3], s[2:3], 0, v[102:103]
	s_lshl_b32 s2, s8, 5
	s_and_b32 s2, s2, 0x7e0
	s_lshl_b32 s3, s21, 11
	s_lshl_b32 s8, s2, 2
	s_or_b32 s2, s3, s2
	v_or_b32_e32 v6, s2, v100
	v_mov_b64_e32 v[4:5], s[10:11]
	v_mad_u64_u32 v[4:5], s[2:3], v6, s7, v[4:5]
	s_mov_b32 s21, s9
	v_readlane_b32 s37, v250, 33
	v_readlane_b32 s38, v250, 34
	v_readlane_b32 s39, v250, 35
	v_readlane_b32 s40, v250, 36
	v_readlane_b32 s41, v250, 37
	v_lshl_add_u64 v[2:3], v[2:3], 0, s[8:9]
	v_lshl_add_u64 v[108:109], v[4:5], 0, s[20:21]
	s_mov_b64 s[2:3], 0

.LBB0_234:
	v_readlane_b32 s2, v250, 40
	v_readlane_b32 s3, v250, 41
	s_cmp_lt_i32 s2, 3
	s_cselect_b64 s[2:3], -1, 0
	s_add_u32 s72, s78, 0x32500000
	s_addc_u32 s73, s79, 0
	s_and_b64 s[0:1], s[2:3], s[0:1]
	s_andn2_b64 vcc, exec, s[0:1]
	s_cbranch_vccnz .LBB0_285
	s_cmp_eq_u32 s97, 0x100
	s_cselect_b32 s98, 184, s97
	v_readfirstlane_b32 s30, v0
	s_lshr_b32 s30, s30, 6
	s_cmp_eq_u32 s97, 0x100
	s_cbranch_scc0 .Lq2_all
	s_cmpk_lt_i32 s74, 184
	s_cbranch_scc1 .Lq2_gemm
	s_sub_u32 s12, s74, 184
	s_lshl_b32 s12, s12, 3
	s_add_u32 s12, s12, s30
	s_add_u32 s12, s12, 0x3000
	s_movk_i32 s13, 576
	s_mov_b32 s14, 0x5328
	s_mov_b32 s46, 2
	s_branch .Lq_conv
.Lq2_all:
	s_lshl_b32 s12, s74, 3
	s_add_u32 s12, s12, s30
	s_add_u32 s12, s12, 0x3000
	s_lshl_b32 s13, s97, 3
	s_mov_b32 s14, 0x5328
	s_mov_b32 s46, 12
	s_branch .Lq_conv
.Lq2_gemm:
	s_cmpk_gt_i32 s74, 0x21f
	v_readfirstlane_b32 s1, v0
	s_cbranch_scc1 .LBB0_251
	v_lshrrev_b32_e32 v2, 5, v0
	v_lshrrev_b32_e32 v4, 1, v0
	v_and_b32_e32 v2, 4, v2
	v_bfe_u32 v3, v0, 2, 2
	v_and_b32_e32 v13, 24, v4
	v_or3_b32 v2, v2, v3, v13
	v_lshlrev_b32_e32 v3, 4, v0
	v_or_b32_e32 v10, 0x2000, v3
	s_add_u32 s30, s78, 0x200000
	v_lshrrev_b32_e32 v4, 7, v10
	s_movk_i32 s0, 0x60
	s_addc_u32 s31, s79, 0
	v_and_or_b32 v5, v4, s0, v2
	v_bfe_u32 v14, v0, 2, 4
	s_movk_i32 s0, 0x70
	s_ashr_i32 s34, s74, 31
	v_and_or_b32 v4, v4, s0, v14
	s_lshr_b32 s0, s34, 29
	s_add_i32 s0, s74, s0
	s_lshr_b32 s10, s1, 6
	s_and_b32 s4, s0, -8
	s_lshr_b32 s12, s1, 8
	s_lshl_b32 s33, s10, 10
	s_sub_i32 s4, s74, s4
	s_cmp_lt_i32 s4, 0
	s_movk_i32 s35, 0x45
	s_cselect_b32 s5, s35, 0x44
	s_mul_i32 s4, s4, s5
	s_ashr_i32 s0, s0, 3
	s_add_i32 s4, s4, s0
	s_mul_hi_i32 s0, s4, 0x78787879
	s_lshr_b32 s5, s0, 31
	s_ashr_i32 s0, s0, 6
	s_add_i32 s0, s0, s5
	s_lshl_b32 s5, s0, 3
	s_mulk_i32 s0, 0x88
	s_sub_i32 s4, s4, s0
	s_sext_i32_i16 s0, s4
	s_bfe_u32 s0, s0, 0x3001c
	s_add_i32 s6, s4, s0
	s_sext_i32_i16 s0, s6
	s_and_b32 s6, s6, 0xfff8
	s_sub_i32 s4, s4, s6
	s_sext_i32_i16 s4, s4
	v_and_b32_e32 v6, 32, v0
	s_lshr_b32 s0, s0, 3
	s_add_i32 s22, s5, s4
	v_bitop3_b32 v11, v3, v6, 48 bitop3:0x6c
	v_and_b32_e32 v12, 64, v0
	s_ashr_i32 s23, s22, 31
	s_bfe_i64 s[6:7], s[0:1], 0x100000
	v_or_b32_e32 v3, v11, v12
	s_lshl_b64 s[4:5], s[22:23], 19
	s_lshl_b64 s[6:7], s[6:7], 19
	v_lshl_or_b32 v164, v4, 11, v3
	v_lshrrev_b32_e32 v4, 3, v0
	s_add_u32 s26, s30, s6
	v_and_or_b32 v2, v4, 32, v2
	s_addc_u32 s27, s31, s7
	s_add_i32 s23, s33, 0
	v_lshl_or_b32 v166, v2, 11, v3
	s_add_i32 m0, s23, 0x10000
	v_lshl_or_b32 v162, v5, 11, v3
	global_load_lds_dwordx4 v166, s[26:27]
	s_add_i32 m0, s23, 0x12000
	s_add_u32 s6, s26, 0x40000
	global_load_lds_dwordx4 v162, s[26:27]
	s_addc_u32 s7, s27, 0
	s_add_i32 m0, s23, 0x14000
	v_and_or_b32 v2, v4, 48, v14
	global_load_lds_dwordx4 v166, s[6:7]
	s_add_i32 m0, s23, 0x16000
	s_add_u32 s24, s72, s4
	s_addc_u32 s25, s73, s5
	s_add_i32 s36, s23, 0x2000
	v_lshl_or_b32 v168, v2, 11, v3
	global_load_lds_dwordx4 v162, s[6:7]
	s_mov_b32 m0, s23
	s_add_u32 s4, s24, 0x40000
	global_load_lds_dwordx4 v168, s[24:25]
	s_mov_b32 m0, s36
	s_addc_u32 s5, s25, 0
	s_add_i32 s37, s23, 0x4000
	v_mov_b32_e32 v1, 0x5cba0000
	global_load_lds_dwordx4 v164, s[24:25]
	s_mov_b32 m0, s37
	s_add_i32 s38, s23, 0x6000
	global_load_dword v1, v1, s[78:79]
	v_mov_b32_e32 v167, 0
	global_load_lds_dwordx4 v168, s[4:5]
	s_mov_b32 m0, s38
	v_mov_b32_e32 v163, v167
	global_load_lds_dwordx4 v164, s[4:5]
	v_mov_b32_e32 v169, v167
	v_mov_b32_e32 v165, v167
	s_cmp_eq_u32 s12, 1
	s_mov_b32 s39, 0
	v_lshl_add_u64 v[8:9], s[26:27], 0, v[166:167]
	v_lshl_add_u64 v[6:7], s[26:27], 0, v[162:163]
	v_lshl_add_u64 v[2:3], s[24:25], 0, v[168:169]
	s_cselect_b64 s[4:5], -1, 0
	s_cmp_lg_u32 s12, 1
	v_lshl_add_u64 v[4:5], s[24:25], 0, v[164:165]
	s_cbranch_scc1 .LBB0_238
	s_barrier

.LBB0_241:
	s_add_i32 s39, s39, 1
	s_mul_i32 s0, s39, s42
	s_mul_hi_u32 s1, s39, s98
	s_add_i32 s1, s1, s0
	s_mul_i32 s0, s39, s98
	s_add_u32 s18, s0, s74
	s_addc_u32 s19, s1, s34
	v_cmp_gt_i64_e32 vcc, s[18:19], v[176:177]
	v_cmp_lt_i64_e64 s[0:1], s[18:19], v[174:175]
	s_cbranch_vccnz .LBB0_243
	s_ashr_i32 s14, s18, 31
	s_lshr_b32 s14, s14, 29
	s_add_i32 s14, s18, s14
	s_ashr_i32 s15, s14, 3
	s_and_b32 s14, s14, -8
	s_sub_i32 s14, s18, s14
	s_cmp_lt_i32 s14, 0
	s_cselect_b32 s16, s35, 0x44
	s_mul_i32 s14, s14, s16
	s_add_i32 s14, s14, s15
	s_mul_hi_i32 s15, s14, 0x78787879
	s_lshr_b32 s16, s15, 31
	s_ashr_i32 s15, s15, 6
	s_add_i32 s15, s15, s16
	s_lshl_b32 s16, s15, 3
	s_sub_i32 s17, 32, s16
	s_min_i32 s17, s17, 8
	s_abs_i32 s18, s17
	v_cvt_f32_u32_e32 v2, s18
	s_sub_i32 s20, 0, s18
	s_mulk_i32 s15, 0x88
	s_sub_i32 s15, s14, s15
	v_rcp_iflag_f32_e32 v2, v2
	s_abs_i32 s14, s15
	s_xor_b32 s19, s15, s17
	s_ashr_i32 s19, s19, 31
	v_mul_f32_e32 v2, 0x4f7ffffe, v2
	v_cvt_u32_f32_e32 v2, v2
	s_nop 0
	v_readfirstlane_b32 s21, v2
	s_mul_i32 s20, s20, s21
	s_mul_hi_u32 s20, s21, s20
	s_add_i32 s21, s21, s20
	s_mul_hi_u32 s20, s14, s21
	s_mul_i32 s21, s20, s18
	s_sub_i32 s14, s14, s21
	s_add_i32 s28, s20, 1
	s_sub_i32 s21, s14, s18
	s_cmp_ge_u32 s14, s18
	s_cselect_b32 s20, s28, s20
	s_cselect_b32 s14, s21, s14
	s_add_i32 s21, s20, 1
	s_cmp_ge_u32 s14, s18
	s_cselect_b32 s14, s21, s20
	s_xor_b32 s14, s14, s19
	s_sub_i32 s14, s14, s19
	s_mul_i32 s17, s14, s17
	s_sub_i32 s15, s15, s17
	s_add_i32 s16, s16, s15

.LBB0_251:
	v_readlane_b32 s0, v250, 44
	v_readlane_b32 s1, v250, 45
	s_andn2_b64 vcc, exec, s[0:1]
	s_cbranch_vccnz .LBB0_285
	s_abs_i32 s0, s97
	v_cvt_f32_u32_e32 v1, s0
	s_sub_i32 s5, 0, s0
	s_add_i32 s1, s97, 0x21f
	s_xor_b32 s4, s1, s97
	v_rcp_iflag_f32_e32 v1, v1
	s_abs_i32 s1, s1
	s_ashr_i32 s4, s4, 31
	v_mul_f32_e32 v1, 0x4f7ffffe, v1
	v_cvt_u32_f32_e32 v1, v1
	s_nop 0
	v_readfirstlane_b32 s6, v1
	s_mul_i32 s5, s5, s6
	s_mul_hi_u32 s5, s6, s5
	s_add_i32 s6, s6, s5
	s_mul_hi_u32 s5, s1, s6
	s_mul_i32 s6, s5, s0
	s_sub_i32 s1, s1, s6
	s_add_i32 s7, s5, 1
	s_sub_i32 s6, s1, s0
	s_cmp_ge_u32 s1, s0
	s_cselect_b32 s5, s7, s5
	s_cselect_b32 s1, s6, s1
	s_add_i32 s6, s5, 1
	s_cmp_ge_u32 s1, s0
	s_cselect_b32 s0, s6, s5
	s_not_b32 s1, s4
	s_xor_b32 s0, s0, s4
	s_add_i32 s0, s1, s0
	s_mul_i32 s0, s0, s97
	s_sub_i32 s4, 0x220, s0
	s_cmp_ge_i32 s4, s97
	s_cselect_b64 s[0:1], -1, 0
	s_cmp_lt_i32 s74, s4
	s_cselect_b64 s[4:5], -1, 0
	s_or_b64 s[0:1], s[0:1], s[4:5]
	s_and_b64 vcc, exec, s[0:1]
	s_cbranch_vccnz .LBB0_285
	s_cmp_gt_i32 s75, -1
	s_cbranch_scc1 .LBB0_285
	v_readlane_b32 s0, v250, 55
	v_and_b32_e32 v2, 7, v0
	v_lshrrev_b32_e32 v3, 3, v178
	s_xor_b32 s14, s0, 0x80000000
	s_cmp_gt_i32 s75, 0xdfff
	v_lshlrev_b32_e32 v1, 4, v3
	v_lshlrev_b32_e32 v134, 2, v2
	v_lshlrev_b32_e32 v2, 4, v2
	s_cbranch_scc0 .LBB0_256
	s_add_i32 s0, s75, 0x2000
	s_bfe_u32 s1, s0, 0x70009
	s_mulk_i32 s1, 0x2493
	s_lshr_b32 s7, s1, 16
	s_mul_i32 s1, s7, 0xe00
	s_sub_i32 s0, s0, s1
	v_readlane_b32 s16, v250, 32
	s_and_b32 s0, s0, 0xffff
	s_mul_i32 s4, s7, 0x3800000
	v_readlane_b32 s22, v250, 38
	v_readlane_b32 s23, v250, 39
	s_add_u32 s4, s22, s4
	s_addc_u32 s5, s23, 0
	s_lshl_b32 s6, s0, 1
	s_and_b32 s6, s6, 0x1f80
	v_lshlrev_b32_e32 v136, 4, v3
	v_or_b32_e32 v3, s6, v136
	v_lshlrev_b32_e32 v4, 13, v3
	v_mov_b32_e32 v5, 0
	s_lshl_b32 s0, s0, 5
	v_lshl_add_u64 v[6:7], s[4:5], 0, v[4:5]
	s_and_b32 s4, s0, 0x7e0
	s_mov_b32 s1, 0
	s_lshl_b32 s0, s4, 2
	v_lshl_add_u64 v[6:7], v[6:7], 0, s[0:1]
	s_lshl_b32 s0, s7, 11
	v_mov_b32_e32 v3, v5
	s_or_b32 s0, s0, s4
	v_mov_b32_e32 v135, v5
	v_lshl_add_u64 v[6:7], v[6:7], 0, v[2:3]
	v_or_b32_e32 v3, s0, v134
	s_movk_i32 s0, 0x1c00
	v_mov_b64_e32 v[4:5], s[78:79]
	v_mad_u64_u32 v[4:5], s[4:5], v3, s0, v[4:5]
	s_mov_b32 s7, s1
	v_lshl_add_u64 v[4:5], v[4:5], 0, s[6:7]
	s_mov_b64 s[0:1], 0x24500000
	v_readlane_b32 s17, v250, 33
	v_readlane_b32 s18, v250, 34
	v_readlane_b32 s19, v250, 35
	v_readlane_b32 s20, v250, 36
	v_readlane_b32 s21, v250, 37
	v_lshl_add_u64 v[66:67], v[4:5], 0, s[0:1]
	s_mov_b64 s[0:1], 0
	s_mov_b32 s15, 0x43000000
	s_branch .LBB0_257

.LBB0_262:
	s_cmp_gt_i32 s17, 0
	s_cselect_b64 s[0:1], -1, 0
	s_cmp_lt_i32 s75, 0
	s_cselect_b64 s[12:13], -1, 0
	s_and_b64 s[12:13], s[0:1], s[12:13]
	v_cndmask_b32_e64 v130, 0, 1, s[12:13]
	v_cmp_ne_u32_e64 s[0:1], 1, v130
	s_andn2_b64 vcc, exec, s[12:13]
	s_cbranch_vccnz .LBB0_269
	s_cmp_gt_i32 s75, 0xdfff
	s_mov_b64 s[10:11], -1
	s_cbranch_scc0 .LBB0_265
	s_add_i32 s10, s75, 0x2000
	s_bfe_u32 s11, s10, 0x70009
	s_mulk_i32 s11, 0x2493
	s_lshr_b32 s13, s11, 16
	s_mul_i32 s11, s13, 0xe00
	s_sub_i32 s10, s10, s11
	v_readlane_b32 s24, v250, 32
	s_and_b32 s21, s10, 0xffff
	s_mul_i32 s10, s13, 0x3800000
	v_readlane_b32 s30, v250, 38
	v_readlane_b32 s31, v250, 39
	s_add_u32 s10, s30, s10
	s_addc_u32 s11, s31, 0
	s_lshl_b32 s12, s21, 1
	s_and_b32 s12, s12, 0x1f80
	s_waitcnt vmcnt(16)
	v_or_b32_e32 v66, s12, v136
	v_lshlrev_b32_e32 v138, 13, v66
	v_lshl_add_u64 v[66:67], s[10:11], 0, v[138:139]
	s_lshl_b32 s10, s21, 5
	s_and_b32 s21, s10, 0x7e0
	s_lshl_b32 s10, s21, 2
	s_mov_b32 s11, s5
	v_lshl_add_u64 v[66:67], v[66:67], 0, s[10:11]
	s_lshl_b32 s10, s13, 11
	s_or_b32 s10, s10, s21
	v_or_b32_e32 v68, s10, v134
	v_mul_hi_i32_i24_e32 v69, 0x1c00, v68
	v_mul_i32_i24_e32 v68, 0x1c00, v68
	v_lshl_add_u64 v[68:69], s[6:7], 0, v[68:69]
	s_mov_b32 s13, s5
	v_readlane_b32 s25, v250, 33
	v_readlane_b32 s26, v250, 34
	v_readlane_b32 s27, v250, 35
	v_readlane_b32 s28, v250, 36
	v_readlane_b32 s29, v250, 37
	v_lshl_add_u64 v[130:131], v[68:69], 0, s[12:13]
	s_mov_b64 s[10:11], 0

.LBB0_273:
	v_mad_u64_u32 v[144:145], s[12:13], s4, 3, v[140:141]
	s_and_b64 vcc, exec, s[0:1]
	s_mov_b64 s[0:1], 0
	global_store_dwordx4 v[144:145], v[130:133], off
	s_cbranch_vccnz .LBB0_261
	s_cmp_gt_i32 s17, 0
	s_cselect_b64 s[0:1], -1, 0
	s_cmp_lt_i32 s75, 0
	s_cselect_b64 s[12:13], -1, 0
	s_and_b64 s[0:1], s[0:1], s[12:13]
	s_andn2_b64 vcc, exec, s[0:1]
	s_cbranch_vccnz .LBB0_281
	s_cmp_gt_i32 s75, 0xdfff
	s_mov_b64 s[12:13], -1
	s_cbranch_scc0 .LBB0_277
	s_add_i32 s4, s75, 0x2000
	s_bfe_u32 s11, s4, 0x70009
	s_mulk_i32 s11, 0x2493
	s_lshr_b32 s11, s11, 16
	s_mul_i32 s12, s11, 0xe00
	s_sub_i32 s4, s4, s12
	v_readlane_b32 s24, v250, 32
	s_and_b32 s4, s4, 0xffff
	s_mul_i32 s12, s11, 0x3800000
	v_readlane_b32 s30, v250, 38
	v_readlane_b32 s31, v250, 39
	s_add_u32 s12, s30, s12
	s_addc_u32 s13, s31, 0
	s_lshl_b32 s15, s4, 1
	s_and_b32 s22, s15, 0x1f80
	s_waitcnt vmcnt(16)
	v_or_b32_e32 v2, s22, v136
	v_lshlrev_b32_e32 v138, 13, v2
	s_lshl_b32 s4, s4, 5
	v_lshl_add_u64 v[2:3], s[12:13], 0, v[138:139]
	s_and_b32 s12, s4, 0x7e0
	s_lshl_b32 s4, s12, 2
	v_lshl_add_u64 v[2:3], v[2:3], 0, s[4:5]
	s_lshl_b32 s4, s11, 11
	s_or_b32 s4, s4, s12
	v_or_b32_e32 v4, s4, v134
	v_mul_hi_i32_i24_e32 v5, 0x1c00, v4
	v_mul_i32_i24_e32 v4, 0x1c00, v4
	v_lshl_add_u64 v[4:5], s[6:7], 0, v[4:5]
	s_mov_b32 s23, s5
	v_readlane_b32 s25, v250, 33
	v_readlane_b32 s26, v250, 34
	v_readlane_b32 s27, v250, 35
	v_readlane_b32 s28, v250, 36
	v_readlane_b32 s29, v250, 37
	v_lshl_add_u64 v[130:131], v[4:5], 0, s[22:23]
	s_mov_b64 s[12:13], 0

.LBB0_346:
	v_writelane_b32 v253, s2, 41
	s_lshl_b32 s2, s81, 4
	s_add_i32 s28, s2, s49
	v_or_b32_e32 v4, s28, v124
	v_mov_b64_e32 v[2:3], s[4:5]
	v_mad_u64_u32 v[4:5], s[2:3], v4, s6, v[2:3]
	v_lshl_add_u64 v[4:5], v[4:5], 0, v[108:109]
	v_or_b32_e32 v107, s28, v101
	v_lshl_add_u64 v[4:5], v[4:5], 0, v[112:113]
	s_mov_b64 s[2:3], 0x1800
	v_lshl_add_u64 v[6:7], v[4:5], 0, s[2:3]
	v_add_co_u32_e32 v4, vcc, 0x1000, v4
	v_mad_u64_u32 v[2:3], s[2:3], v107, s6, v[2:3]
	s_nop 0
	v_addc_co_u32_e32 v5, vcc, 0, v5, vcc
	s_mov_b64 s[2:3], 0x2080
	global_load_dwordx4 v[18:21], v[6:7], off offset:32
	global_load_dwordx4 v[22:25], v[6:7], off offset:64
	global_load_dwordx4 v[26:29], v[4:5], off offset:2048
	global_load_dwordx4 v[30:33], v[6:7], off offset:96
	v_lshl_add_u64 v[4:5], v[2:3], 0, s[2:3]
	v_add_co_u32_e32 v2, vcc, 0x2000, v2
	v_writelane_b32 v253, s4, 43
	s_nop 0
	v_addc_co_u32_e32 v3, vcc, 0, v3, vcc
	global_load_dwordx4 v[6:9], v[2:3], off offset:128
	s_nop 0
	global_load_dwordx4 v[2:5], v[4:5], off offset:16
	s_cmp_gt_i32 s75, 0x2fff
	v_writelane_b32 v253, s5, 44
	s_cbranch_scc1 .LBB0_357
	s_cmp_gt_i32 s75, 0xdfff
	s_mov_b64 s[2:3], -1
	s_cbranch_scc0 .LBB0_349
	s_add_i32 s2, s75, 0x2000
	s_bfe_u32 s3, s2, 0x70009
	s_mulk_i32 s3, 0x2493
	s_lshr_b32 s5, s3, 16
	s_mul_i32 s3, s5, 0xe00
	s_sub_i32 s2, s2, s3
	s_and_b32 s6, s2, 0xffff
	s_mul_i32 s2, s5, 0x3800000
	s_add_u32 s2, s22, s2
	s_addc_u32 s3, s23, 0
	s_lshl_b32 s4, s6, 1
	s_and_b32 s4, s4, 0x1f80
	v_or_b32_e32 v10, s4, v98
	v_lshlrev_b32_e32 v96, 13, v10
	v_lshl_add_u64 v[10:11], s[2:3], 0, v[96:97]
	s_lshl_b32 s2, s6, 5
	s_and_b32 s2, s2, 0x7e0
	s_lshl_b32 s3, s5, 11
	s_lshl_b32 s68, s2, 2
	s_or_b32 s2, s3, s2
	v_or_b32_e32 v14, s2, v100
	v_readlane_b32 s2, v251, 22
	v_readlane_b32 s3, v251, 23
	s_mov_b32 s5, s69
	v_lshl_add_u64 v[10:11], v[10:11], 0, s[68:69]
	v_mov_b64_e32 v[12:13], s[2:3]
	s_movk_i32 s2, 0x1c00
	v_mad_u64_u32 v[12:13], s[2:3], v14, s2, v[12:13]
	v_lshl_add_u64 v[90:91], v[12:13], 0, s[4:5]
	s_mov_b64 s[2:3], 0

.LBB0_369:
	s_cmp_lt_i32 s75, 0x3000
	s_cselect_b64 s[8:9], -1, 0
	s_and_b64 vcc, exec, s[8:9]
	v_writelane_b32 v253, s75, 45
	s_cbranch_vccz .LBB0_374
	s_cmp_gt_i32 s75, 0xdfff
	s_mov_b64 s[0:1], -1
	s_cbranch_scc0 .LBB0_372
	s_add_i32 s0, s75, 0x2000
	s_bfe_u32 s1, s0, 0x70009
	s_mulk_i32 s1, 0x2493
	s_lshr_b32 s3, s1, 16
	s_mul_i32 s1, s3, 0xe00
	s_sub_i32 s0, s0, s1
	s_and_b32 s4, s0, 0xffff
	s_mul_i32 s0, s3, 0x3800000
	s_add_u32 s0, s22, s0
	s_addc_u32 s1, s23, 0
	s_lshl_b32 s2, s4, 1
	s_and_b32 s2, s2, 0x1f80
	v_or_b32_e32 v2, s2, v98
	v_lshlrev_b32_e32 v96, 13, v2
	v_lshl_add_u64 v[2:3], s[0:1], 0, v[96:97]
	s_lshl_b32 s0, s4, 5
	s_and_b32 s0, s0, 0x7e0
	s_lshl_b32 s1, s3, 11
	s_lshl_b32 s68, s0, 2
	s_or_b32 s0, s1, s0
	v_or_b32_e32 v6, s0, v100
	v_readlane_b32 s0, v251, 22
	v_readlane_b32 s1, v251, 23
	s_mov_b32 s3, s69
	v_lshl_add_u64 v[2:3], v[2:3], 0, s[68:69]
	v_mov_b64_e32 v[4:5], s[0:1]
	s_movk_i32 s0, 0x1c00
	v_mad_u64_u32 v[4:5], s[0:1], v6, s0, v[4:5]
	v_lshl_add_u64 v[66:67], v[4:5], 0, s[2:3]
	s_mov_b64 s[0:1], 0

.LBB0_394:
	v_writelane_b32 v253, s28, 51
	s_waitcnt vmcnt(0)
	v_mov_b32_e32 v2, s39
	v_mov_b32_e32 v3, s37
	v_writelane_b32 v253, s29, 52
	v_writelane_b32 v253, s26, 53
	v_readlane_b32 s70, v252, 56
	v_readlane_b32 s71, v252, 57
	v_writelane_b32 v253, s27, 54
	v_writelane_b32 v253, s68, 55
	v_readlane_b32 s74, v252, 54
	v_readlane_b32 s75, v252, 55
	v_writelane_b32 v253, s69, 56
	s_mov_b64 vcc, s[18:19]
	v_readlane_b32 s40, v253, 30
	v_readlane_b32 s41, v253, 31
	v_writelane_b32 v253, s38, 57
	v_readlane_b32 s18, v252, 52
	v_cndmask_b32_e64 v2, 0, v2, s[40:41]
	v_writelane_b32 v253, s39, 58
	v_readlane_b32 s19, v252, 53
	v_readlane_b32 s38, v253, 28
	v_readlane_b32 s39, v253, 29
	v_writelane_b32 v253, s36, 59
	s_mov_b32 s52, s86
	v_cndmask_b32_e64 v2, v2, v3, s[38:39]
	v_writelane_b32 v253, s37, 60
	v_mov_b32_e32 v3, s35
	v_readlane_b32 s36, v253, 26
	v_readlane_b32 s37, v253, 27
	v_writelane_b32 v253, s34, 61
	v_readlane_b32 s84, v252, 46
	v_cndmask_b32_e64 v2, v2, v3, s[36:37]
	v_writelane_b32 v253, s35, 62
	v_mov_b32_e32 v3, s97
	v_readlane_b32 s34, v253, 24
	v_readlane_b32 s35, v253, 25
	v_readlane_b32 s85, v252, 47
	s_mov_b32 s80, s72
	v_cndmask_b32_e64 v2, v2, v3, s[34:35]
	v_mov_b32_e32 v3, s31
	v_writelane_b32 v253, s30, 63
	s_mov_b64 s[76:77], s[94:95]
	v_readlane_b32 s28, v253, 20
	v_writelane_b32 v254, s31, 0
	v_readlane_b32 s30, v253, 22
	v_readlane_b32 s31, v253, 23
	v_readlane_b32 s29, v253, 21
	v_readlane_b32 s26, v253, 18
	v_cndmask_b32_e64 v2, v2, v3, s[30:31]
	v_mov_b32_e32 v3, s51
	v_cndmask_b32_e64 v2, v2, v3, s[28:29]
	v_mov_b32_e32 v3, s91
	v_readlane_b32 s27, v253, 19
	v_readlane_b32 s0, v253, 10
	v_readlane_b32 s1, v253, 11
	v_cndmask_b32_e64 v2, v2, v3, s[26:27]
	v_mov_b32_e32 v3, s25
	v_writelane_b32 v254, s24, 1
	v_readlane_b32 s14, v253, 6
	v_readlane_b32 s15, v253, 7
	v_writelane_b32 v254, s25, 2
	v_readlane_b32 s24, v253, 16
	v_readlane_b32 s25, v253, 17
	v_readlane_b32 s8, v253, 0
	v_readlane_b32 s9, v253, 1
	v_cndmask_b32_e64 v2, v2, v3, s[24:25]
	v_mov_b32_e32 v3, s23
	v_writelane_b32 v254, s22, 3
	v_readlane_b32 s68, v252, 42
	v_readlane_b32 s69, v252, 43
	v_writelane_b32 v254, s23, 4
	v_readlane_b32 s22, v253, 14
	v_readlane_b32 s23, v253, 15
	v_readlane_b32 s92, v252, 40
	v_readlane_b32 s93, v252, 41
	v_cndmask_b32_e64 v2, v2, v3, s[22:23]
	v_mov_b32_e32 v3, s21
	v_writelane_b32 v254, s20, 5
	v_readlane_b32 s94, v252, 38
	v_readlane_b32 s95, v252, 39
	v_writelane_b32 v254, s21, 6
	v_readlane_b32 s20, v253, 12
	v_readlane_b32 s21, v253, 13
	v_readlane_b32 s66, v252, 36
	v_readlane_b32 s67, v252, 37
	v_cndmask_b32_e64 v2, v2, v3, s[20:21]
	v_mov_b32_e32 v3, s89
	v_cndmask_b32_e64 v2, v2, v3, s[0:1]
	v_mov_b32_e32 v3, s17
	v_writelane_b32 v254, s16, 7
	s_mov_b32 s48, s82
	v_readlane_b32 s78, v253, 57
	v_writelane_b32 v254, s17, 8
	v_readlane_b32 s16, v253, 8
	v_readlane_b32 s17, v253, 9
	v_lshlrev_b32_e32 v122, 2, v178
	v_mov_b32_e32 v107, v97
	v_cndmask_b32_e64 v2, v2, v3, s[16:17]
	v_mov_b32_e32 v3, s87
	v_cndmask_b32_e64 v2, v2, v3, s[14:15]
	v_mov_b32_e32 v3, s13
	v_writelane_b32 v254, s12, 9
	v_readlane_b32 s86, v252, 48
	v_readlane_b32 s87, v252, 49
	v_writelane_b32 v254, s13, 10
	v_readlane_b32 s12, v253, 4
	v_readlane_b32 s13, v253, 5
	v_mov_b32_e32 v111, v97
	v_readlane_b32 s79, v253, 58
	v_cndmask_b32_e64 v2, v2, v3, s[12:13]
	v_mov_b32_e32 v3, s11
	v_writelane_b32 v254, s10, 11
	s_nop 1
	v_writelane_b32 v254, s11, 12
	v_readlane_b32 s10, v253, 2
	v_readlane_b32 s11, v253, 3
	s_nop 1
	v_cndmask_b32_e64 v2, v2, v3, s[10:11]
	v_mov_b32_e32 v3, s45
	v_cndmask_b32_e64 v2, v2, v3, s[8:9]
	v_mov_b32_e32 v3, s7
	v_writelane_b32 v254, s6, 13
	s_nop 1
	v_writelane_b32 v254, s7, 14
	v_readlane_b32 s6, v252, 62
	v_readlane_b32 s7, v252, 63
	s_nop 1
	v_cndmask_b32_e64 v2, v2, v3, s[6:7]
	v_mov_b32_e32 v3, s5
	v_writelane_b32 v254, s4, 15
	s_nop 1
	v_writelane_b32 v254, s5, 16
	v_readlane_b32 s4, v252, 60
	v_writelane_b32 v254, s44, 17
	v_readlane_b32 s5, v252, 61
	s_nop 0
	v_writelane_b32 v254, s45, 18
	v_cndmask_b32_e64 v2, v2, v3, s[4:5]
	v_mov_b32_e32 v3, s3
	v_writelane_b32 v254, s2, 19
	s_mov_b32 s44, s88
	v_readlane_b32 s88, v252, 50
	v_writelane_b32 v254, s3, 20
	v_readlane_b32 s2, v252, 58
	v_readlane_b32 s3, v252, 59
	v_readlane_b32 s89, v252, 51
	v_writelane_b32 v254, s42, 21
	v_cndmask_b32_e64 v2, v2, v3, s[2:3]
	v_mov_b32_e32 v3, s83
	v_cndmask_b32_e64 v2, v2, v3, s[70:71]
	v_mov_b32_e32 v3, s73
	v_cndmask_b32_e64 v2, v2, v3, s[74:75]
	v_mov_b32_e32 v3, vcc_hi
	v_cndmask_b32_e64 v2, v2, v3, s[18:19]
	v_mov_b32_e32 v3, s63
	v_cndmask_b32_e64 v2, v2, v3, s[88:89]
	v_mov_b32_e32 v3, s61
	v_cndmask_b32_e64 v2, v2, v3, s[86:87]
	v_mov_b32_e32 v3, s59
	v_readlane_b32 s72, v252, 44
	v_cndmask_b32_e64 v2, v2, v3, s[84:85]
	v_mov_b32_e32 v3, s57
	v_readlane_b32 s73, v252, 45
	v_writelane_b32 v254, s43, 22
	v_readlane_b32 s82, v252, 34
	v_cndmask_b32_e64 v2, v2, v3, s[72:73]
	v_mov_b32_e32 v3, s77
	v_cndmask_b32_e64 v2, v2, v3, s[68:69]
	v_mov_b32_e32 v3, s43
	v_cndmask_b32_e64 v2, v2, v3, s[92:93]
	v_mov_b32_e32 v3, s65
	v_cndmask_b32_e64 v2, v2, v3, s[94:95]
	v_mov_b32_e32 v3, s55
	v_writelane_b32 v254, s54, 23
	v_cndmask_b32_e64 v2, v2, v3, s[66:67]
	v_mov_b32_e32 v3, s47
	v_writelane_b32 v254, s55, 24
	v_writelane_b32 v254, s64, 25
	v_readlane_b32 s83, v252, 35
	v_readlane_b32 s54, v253, 49
	v_writelane_b32 v254, s65, 26
	v_writelane_b32 v254, s46, 27
	s_mov_b32 s64, vcc_lo
	v_readlane_b32 vcc_lo, v252, 32
	v_writelane_b32 v254, s47, 28
	v_readlane_b32 s46, v253, 47
	v_readlane_b32 s47, v253, 48
	v_cndmask_b32_e64 v2, v2, v3, s[82:83]
	v_readlane_b32 vcc_hi, v252, 33
	v_mov_b32_e32 v3, s47
	s_mov_b32 s42, s76
	v_readlane_b32 s55, v253, 50
	v_readlane_b32 s76, v252, 23
	v_cndmask_b32_e32 v2, v2, v3, vcc
	v_mov_b32_e32 v3, s55
	v_readlane_b32 s77, v252, 24
	s_nop 1
	v_cndmask_b32_e64 v2, v2, v3, s[76:77]
	v_mov_b32_e32 v3, s78
	v_cndmask_b32_e64 v3, 0, v3, s[40:41]
	v_readlane_b32 s40, v253, 59
	v_readlane_b32 s41, v253, 60
	s_nop 0
	v_mov_b32_e32 v4, s40
	v_cndmask_b32_e64 v3, v3, v4, s[38:39]
	v_readlane_b32 s38, v253, 61
	v_readlane_b32 s39, v253, 62
	s_nop 0
	v_mov_b32_e32 v4, s38
	v_cndmask_b32_e64 v3, v3, v4, s[36:37]
	v_mov_b32_e32 v4, s96
	v_cndmask_b32_e64 v3, v3, v4, s[34:35]
	v_readlane_b32 s34, v253, 63
	v_readlane_b32 s35, v254, 0
	s_nop 0
	v_mov_b32_e32 v4, s34
	v_cndmask_b32_e64 v3, v3, v4, s[30:31]
	v_mov_b32_e32 v4, s50
	v_cndmask_b32_e64 v3, v3, v4, s[28:29]
	v_mov_b32_e32 v4, s90
	v_cndmask_b32_e64 v3, v3, v4, s[26:27]
	v_readlane_b32 s26, v254, 1
	v_readlane_b32 s27, v254, 2
	s_nop 0
	v_mov_b32_e32 v4, s26
	v_cndmask_b32_e64 v3, v3, v4, s[24:25]
	v_readlane_b32 s24, v254, 3
	v_readlane_b32 s25, v254, 4
	s_nop 0
	v_mov_b32_e32 v4, s24
	v_cndmask_b32_e64 v3, v3, v4, s[22:23]
	v_readlane_b32 s22, v254, 5
	v_readlane_b32 s23, v254, 6
	s_nop 0
	v_mov_b32_e32 v4, s22
	v_cndmask_b32_e64 v3, v3, v4, s[20:21]
	v_mov_b32_e32 v4, s44
	v_cndmask_b32_e64 v3, v3, v4, s[0:1]
	v_readlane_b32 s0, v254, 7
	v_readlane_b32 s1, v254, 8
	s_nop 0
	v_mov_b32_e32 v4, s0
	v_readlane_b32 s0, v254, 9
	v_cndmask_b32_e64 v3, v3, v4, s[16:17]
	v_mov_b32_e32 v4, s52
	v_readlane_b32 s1, v254, 10
	v_cndmask_b32_e64 v3, v3, v4, s[14:15]
	v_mov_b32_e32 v4, s0
	v_readlane_b32 s0, v254, 11
	v_readlane_b32 s1, v254, 12
	v_cndmask_b32_e64 v3, v3, v4, s[12:13]
	v_mov_b32_e32 v4, s0
	v_readlane_b32 s0, v254, 17
	v_readlane_b32 s1, v254, 18
	v_cndmask_b32_e64 v3, v3, v4, s[10:11]
	v_mov_b32_e32 v4, s0
	v_readlane_b32 s0, v254, 13
	v_readlane_b32 s1, v254, 14
	v_cndmask_b32_e64 v3, v3, v4, s[8:9]
	v_mov_b32_e32 v4, s0
	v_readlane_b32 s0, v254, 15
	v_readlane_b32 s1, v254, 16
	v_cndmask_b32_e64 v3, v3, v4, s[6:7]
	v_mov_b32_e32 v4, s0
	v_readlane_b32 s0, v254, 19
	v_cndmask_b32_e64 v3, v3, v4, s[4:5]
	v_readlane_b32 s1, v254, 20
	v_mov_b32_e32 v4, s0
	v_cndmask_b32_e64 v3, v3, v4, s[2:3]
	v_mov_b32_e32 v4, s48
	v_cndmask_b32_e64 v3, v3, v4, s[70:71]
	v_mov_b32_e32 v4, s80
	v_cndmask_b32_e64 v3, v3, v4, s[74:75]
	v_mov_b32_e32 v4, s64
	v_cndmask_b32_e64 v3, v3, v4, s[18:19]
	v_mov_b32_e32 v4, s62
	v_cndmask_b32_e64 v3, v3, v4, s[88:89]
	v_mov_b32_e32 v4, s60
	v_cndmask_b32_e64 v3, v3, v4, s[86:87]
	v_mov_b32_e32 v4, s58
	v_cndmask_b32_e64 v3, v3, v4, s[84:85]
	v_mov_b32_e32 v4, s56
	v_readlane_b32 s0, v254, 21
	v_cndmask_b32_e64 v3, v3, v4, s[72:73]
	v_mov_b32_e32 v4, s42
	v_readlane_b32 s1, v254, 22
	v_cndmask_b32_e64 v3, v3, v4, s[68:69]
	v_mov_b32_e32 v4, s0
	v_readlane_b32 s0, v254, 25
	v_readlane_b32 s1, v254, 26
	v_cndmask_b32_e64 v3, v3, v4, s[92:93]
	v_mov_b32_e32 v4, s0
	v_readlane_b32 s0, v254, 23
	v_readlane_b32 s1, v254, 24
	v_cndmask_b32_e64 v3, v3, v4, s[94:95]
	v_mov_b32_e32 v4, s0
	v_readlane_b32 s0, v254, 27
	v_readlane_b32 s1, v254, 28
	v_readlane_b32 s18, v253, 55
	v_readlane_b32 s2, v253, 51
	v_cndmask_b32_e64 v3, v3, v4, s[66:67]
	v_mov_b32_e32 v4, s0
	v_readlane_b32 s19, v253, 56
	v_readlane_b32 s3, v253, 52
	v_readlane_b32 s0, v253, 53
	s_mov_b32 s3, s19
	v_readlane_b32 s1, v253, 54
	s_lshl_b64 s[0:1], s[0:1], 19
	s_lshl_b64 s[2:3], s[2:3], 8
	v_readlane_b32 s4, v252, 25
	s_add_u32 s4, s4, s0
	v_readlane_b32 s0, v252, 26
	v_cndmask_b32_e64 v3, v3, v4, s[82:83]
	v_mov_b32_e32 v4, s46
	s_addc_u32 s1, s0, s1
	v_cndmask_b32_e32 v3, v3, v4, vcc
	v_mov_b32_e32 v4, s54
	v_writelane_b32 v254, s4, 19
	s_add_u32 s0, s4, s2
	v_cndmask_b32_e64 v3, v3, v4, s[76:77]
	v_writelane_b32 v254, s1, 27
	s_addc_u32 s1, s1, s3
	s_xor_b32 s6, s81, 0x7f
	global_store_dword v122, v3, s[0:1]
	global_store_dword v122, v2, s[0:1] offset:256
	s_lshl_b32 s0, s6, 4
	v_readlane_b32 s1, v253, 39
	s_add_i32 s0, s0, s49
	s_mov_b32 m0, s1
	v_readlane_b32 s1, v253, 41
	v_or_b32_e32 v146, s0, v101
	global_load_lds_dwordx4 v[116:117], off
	s_add_i32 m0, s1, 0x22400
	s_mov_b32 s2, s0
	v_or_b32_e32 v4, s0, v124
	v_readlane_b32 s0, v253, 43
	v_writelane_b32 v254, s2, 23
	v_readlane_b32 s1, v253, 44
	global_load_lds_dwordx4 v[118:119], off
	v_writelane_b32 v254, s3, 24
	v_mov_b64_e32 v[2:3], s[0:1]
	s_movk_i32 s2, 0x2200
	v_mad_u64_u32 v[4:5], s[0:1], v4, s2, v[2:3]
	v_lshl_add_u64 v[4:5], v[4:5], 0, v[106:107]
	v_lshl_add_u64 v[4:5], v[4:5], 0, v[110:111]
	s_mov_b64 s[0:1], 0x1800
	v_lshl_add_u64 v[6:7], v[4:5], 0, s[0:1]
	s_movk_i32 s0, 0x1000
	v_add_co_u32_e32 v4, vcc, s0, v4
	v_mad_u64_u32 v[2:3], s[0:1], v146, s2, v[2:3]
	s_nop 0
	v_addc_co_u32_e32 v5, vcc, 0, v5, vcc
	s_mov_b64 s[0:1], 0x2080
	global_load_dwordx4 v[18:21], v[4:5], off offset:2048
	global_load_dwordx4 v[22:25], v[6:7], off offset:32
	global_load_dwordx4 v[26:29], v[6:7], off offset:64
	global_load_dwordx4 v[30:33], v[6:7], off offset:96
	v_lshl_add_u64 v[4:5], v[2:3], 0, s[0:1]
	v_add_co_u32_e32 v2, vcc, 0x2000, v2
	v_readlane_b32 s83, v253, 45
	s_nop 0
	v_addc_co_u32_e32 v3, vcc, 0, v3, vcc
	global_load_dwordx4 v[6:9], v[2:3], off offset:128
	s_nop 0
	global_load_dwordx4 v[2:5], v[4:5], off offset:16
	s_cmp_gt_i32 s83, 0x2fff
	s_cbranch_scc1 .LBB0_399
	v_readlane_b32 s84, v250, 32
	s_cmp_gt_i32 s83, 0xdfff
	s_mov_b64 s[0:1], -1
	v_readlane_b32 s86, v250, 34
	v_readlane_b32 s87, v250, 35
	v_readlane_b32 s88, v250, 36
	v_readlane_b32 s89, v250, 37
	v_readlane_b32 s90, v250, 38
	v_readlane_b32 s91, v250, 39
	s_movk_i32 s14, 0x100
	v_readlane_b32 s16, v250, 53
	s_mov_b64 s[12:13], 0x88000
	v_readlane_b32 s92, v253, 35
	v_readlane_b32 s85, v250, 33
	v_readlane_b32 s17, v250, 54
	v_readlane_b32 s93, v253, 36
	s_cbranch_scc0 .LBB0_397
	s_add_i32 s0, s83, 0x2000
	s_bfe_u32 s1, s0, 0x70009
	s_mulk_i32 s1, 0x2493
	s_lshr_b32 s3, s1, 16
	s_mul_i32 s1, s3, 0xe00
	s_sub_i32 s0, s0, s1
	s_and_b32 s4, s0, 0xffff
	s_mul_i32 s0, s3, 0x3800000
	s_add_u32 s0, s90, s0
	s_addc_u32 s1, s91, 0
	s_lshl_b32 s2, s4, 1
	s_and_b32 s2, s2, 0x1f80
	v_or_b32_e32 v10, s2, v98
	v_lshlrev_b32_e32 v96, 13, v10
	v_lshl_add_u64 v[10:11], s[0:1], 0, v[96:97]
	s_lshl_b32 s0, s4, 5
	s_and_b32 s0, s0, 0x7e0
	s_lshl_b32 s1, s3, 11
	s_lshl_b32 s18, s0, 2
	s_or_b32 s0, s1, s0
	v_or_b32_e32 v14, s0, v100
	v_readlane_b32 s0, v251, 22
	v_readlane_b32 s1, v251, 23
	s_mov_b32 s3, s19
	v_lshl_add_u64 v[10:11], v[10:11], 0, s[18:19]
	v_mov_b64_e32 v[12:13], s[0:1]
	s_movk_i32 s0, 0x1c00
	v_mad_u64_u32 v[12:13], s[0:1], v14, s0, v[12:13]
	v_lshl_add_u64 v[90:91], v[12:13], 0, s[2:3]
	s_mov_b64 s[0:1], 0

.LBB0_418:
	s_cmp_lt_i32 s83, 0x3000
	s_cselect_b64 s[4:5], -1, 0
	s_and_b64 vcc, exec, s[4:5]
	s_cbranch_vccz .LBB0_423
	s_cmp_gt_i32 s83, 0xdfff
	s_mov_b64 s[0:1], -1
	s_cbranch_scc0 .LBB0_421
	s_add_i32 s0, s83, 0x2000
	s_bfe_u32 s1, s0, 0x70009
	s_mulk_i32 s1, 0x2493
	s_lshr_b32 s3, s1, 16
	s_mul_i32 s1, s3, 0xe00
	s_sub_i32 s0, s0, s1
	s_and_b32 s7, s0, 0xffff
	s_mul_i32 s0, s3, 0x3800000
	s_add_u32 s0, s90, s0
	s_addc_u32 s1, s91, 0
	s_lshl_b32 s8, s7, 1
	s_and_b32 s8, s8, 0x1f80
	v_or_b32_e32 v2, s8, v98
	v_lshlrev_b32_e32 v96, 13, v2
	v_lshl_add_u64 v[2:3], s[0:1], 0, v[96:97]
	s_lshl_b32 s0, s7, 5
	s_and_b32 s0, s0, 0x7e0
	s_lshl_b32 s1, s3, 11
	s_lshl_b32 s18, s0, 2
	s_or_b32 s0, s1, s0
	v_or_b32_e32 v6, s0, v100
	v_readlane_b32 s0, v251, 22
	v_readlane_b32 s1, v251, 23
	s_mov_b32 s9, s19
	v_lshl_add_u64 v[2:3], v[2:3], 0, s[18:19]
	v_mov_b64_e32 v[4:5], s[0:1]
	s_movk_i32 s0, 0x1c00
	v_mad_u64_u32 v[4:5], s[0:1], v6, s0, v[4:5]
	v_lshl_add_u64 v[66:67], v[4:5], 0, s[8:9]
	s_mov_b64 s[0:1], 0

.LBB0_517:
	s_or_b64 exec, exec, s[6:7]
	s_and_saveexec_b64 s[4:5], s[0:1]
	v_mov_b32_e32 v2, s49
	ds_write_b32 v2, v205
	s_or_b64 exec, exec, s[4:5]
	s_add_i32 s59, s59, s40
	s_ashr_i32 s4, s59, 31
	s_add_u32 s5, s59, s39
	s_addc_u32 s4, s4, 0
	v_mov_b32_e32 v69, s4
	v_or_b32_e32 v68, s5, v118
	s_lshl_b32 s4, s58, 9
	v_lshlrev_b64 v[4:5], 12, v[68:69]
	s_or_b32 s30, s4, s41
	v_lshl_add_u64 v[4:5], s[10:11], 0, v[4:5]
	s_lshl_b32 s16, s30, 1
	v_lshl_add_u64 v[4:5], v[4:5], 0, s[16:17]
	v_lshlrev_b32_e32 v2, 1, v122
	v_lshl_add_u64 v[4:5], v[4:5], 0, v[2:3]
	global_load_dwordx4 v[86:89], v[4:5], off
	global_load_dwordx4 v[90:93], v[4:5], off offset:32
	global_load_dwordx4 v[94:97], v[4:5], off offset:64
	global_load_dwordx4 v[98:101], v[4:5], off offset:96
	global_load_dwordx4 v[102:105], v[4:5], off offset:128
	global_load_dwordx4 v[106:109], v[4:5], off offset:160
	global_load_dwordx4 v[110:113], v[4:5], off offset:192
	global_load_dwordx4 v[114:117], v[4:5], off offset:224
	s_cmp_lt_i32 s75, 0x3000
	s_cselect_b64 s[6:7], -1, 0
	s_cmp_gt_i32 s75, 0x2fff
	s_cbranch_scc1 .LBB0_524
	s_cmp_gt_i32 s75, 0xdfff
	s_mov_b64 s[4:5], -1
	s_cbranch_scc0 .LBB0_522
	s_add_i32 s4, s75, 0x2000
	s_bfe_u32 s5, s4, 0x70009
	s_mulk_i32 s5, 0x2493
	s_lshr_b32 s31, s5, 16
	s_mul_i32 s5, s31, 0xe00
	s_sub_i32 s4, s4, s5
	v_readlane_b32 s64, v250, 32
	s_and_b32 s16, s4, 0xffff
	s_mul_i32 s4, s31, 0x3800000
	v_readlane_b32 s70, v250, 38
	v_readlane_b32 s71, v250, 39
	s_add_u32 s4, s70, s4
	s_addc_u32 s5, s71, 0
	s_lshl_b32 s34, s16, 1
	s_and_b32 s34, s34, 0x1f80
	v_or_b32_e32 v2, s34, v124
	v_lshlrev_b32_e32 v2, 13, v2
	v_lshl_add_u64 v[4:5], s[4:5], 0, v[2:3]
	s_lshl_b32 s4, s16, 5
	s_and_b32 s4, s4, 0x7e0
	s_lshl_b32 s5, s31, 11
	s_lshl_b32 s16, s4, 2
	s_or_b32 s4, s5, s4
	v_readlane_b32 s68, v250, 36
	v_readlane_b32 s69, v250, 37
	v_or_b32_e32 v2, s4, v182
	v_mov_b64_e32 v[6:7], s[18:19]
	s_movk_i32 s4, 0x1c00
	v_readlane_b32 s68, v251, 13
	v_mad_u64_u32 v[6:7], s[4:5], v2, s4, v[6:7]
	s_mov_b32 s35, s17
	v_readlane_b32 s65, v250, 33
	v_readlane_b32 s66, v250, 34
	v_readlane_b32 s67, v250, 35
	v_readlane_b32 s69, v251, 14
	v_lshl_add_u64 v[4:5], v[4:5], 0, s[16:17]
	v_lshl_add_u64 v[70:71], v[6:7], 0, s[34:35]
	s_mov_b64 s[4:5], 0

.LBB0_688:
	global_load_dwordx4 v[94:97], v[102:103], off offset:-4096
	global_load_dwordx4 v[90:93], v[102:103], off offset:-3072
	global_load_dwordx4 v[86:89], v[102:103], off offset:-2048
	global_load_dwordx4 v[82:85], v[102:103], off offset:-1024
	global_load_dwordx4 v[78:81], v[102:103], off
	global_load_dwordx4 v[74:77], v[102:103], off offset:1024
	global_load_dwordx4 v[70:73], v[102:103], off offset:2048
	global_load_dwordx4 v[66:69], v[102:103], off offset:3072
	s_cmp_lt_i32 s75, 0x3000
	s_cselect_b64 s[22:23], -1, 0
	s_cmp_gt_i32 s75, 0x2fff
	s_cbranch_scc1 .LBB0_693
	s_cmp_gt_i32 s75, 0xdfff
	s_mov_b64 s[2:3], -1
	s_cbranch_scc0 .LBB0_691
	s_add_i32 s2, s75, 0x2000
	s_bfe_u32 s3, s2, 0x70009
	s_mulk_i32 s3, 0x2493
	s_lshr_b32 s21, s3, 16
	s_mul_i32 s3, s21, 0xe00
	s_sub_i32 s2, s2, s3
	v_readlane_b32 s36, v250, 32
	s_and_b32 s8, s2, 0xffff
	s_mul_i32 s2, s21, 0x3800000
	v_readlane_b32 s42, v250, 38
	v_readlane_b32 s43, v250, 39
	s_add_u32 s2, s42, s2
	s_addc_u32 s3, s43, 0
	s_lshl_b32 s20, s8, 1
	s_and_b32 s20, s20, 0x1f80
	v_or_b32_e32 v2, s20, v98
	v_lshlrev_b32_e32 v100, 13, v2
	v_lshl_add_u64 v[2:3], s[2:3], 0, v[100:101]
	s_lshl_b32 s2, s8, 5
	s_and_b32 s2, s2, 0x7e0
	s_lshl_b32 s3, s21, 11
	s_lshl_b32 s8, s2, 2
	s_or_b32 s2, s3, s2
	v_or_b32_e32 v6, s2, v182
	v_mov_b64_e32 v[4:5], s[10:11]
	v_mad_u64_u32 v[4:5], s[2:3], v6, s7, v[4:5]
	s_mov_b32 s21, s9
	v_readlane_b32 s37, v250, 33
	v_readlane_b32 s38, v250, 34
	v_readlane_b32 s39, v250, 35
	v_readlane_b32 s40, v250, 36
	v_readlane_b32 s41, v250, 37
	v_lshl_add_u64 v[2:3], v[2:3], 0, s[8:9]
	v_lshl_add_u64 v[106:107], v[4:5], 0, s[20:21]
	s_mov_b64 s[2:3], 0

.LBB0_753:
	s_or_b64 exec, exec, s[2:3]
	s_waitcnt lgkmcnt(0)
	s_barrier
	s_branch .Lq_skip
.Lq_conv:
	v_and_b32_e32 v150, 63, v0
	v_lshrrev_b32_e32 v151, 3, v150
	v_and_b32_e32 v152, 7, v150
	v_mul_u32_u24_e32 v130, 0x70000, v151
	v_lshl_add_u32 v130, v152, 4, v130
	v_add_u32_e32 v131, 0x7000, v130
	v_add_u32_e32 v132, 0xe000, v130
	v_add_u32_e32 v133, 0x15000, v130
	v_add_u32_e32 v134, 0x1c000, v130
	v_add_u32_e32 v135, 0x23000, v130
	v_add_u32_e32 v136, 0x2a000, v130
	v_add_u32_e32 v137, 0x31000, v130
	v_add_u32_e32 v138, 0x38000, v130
	v_add_u32_e32 v139, 0x3f000, v130
	v_add_u32_e32 v140, 0x46000, v130
	v_add_u32_e32 v141, 0x4d000, v130
	v_add_u32_e32 v142, 0x54000, v130
	v_add_u32_e32 v143, 0x5b000, v130
	v_add_u32_e32 v144, 0x62000, v130
	v_add_u32_e32 v145, 0x69000, v130
	v_lshlrev_b32_e32 v146, 4, v151
	v_lshl_add_u32 v146, v152, 13, v146
	v_add_u32_e32 v147, 0x800, v146
	v_add_u32_e32 v148, 0x1000, v146
	v_add_u32_e32 v149, 0x1800, v146
	v_mov_b32_e32 v166, 0x4b400000
	v_mov_b32_e32 v167, 0x4b40007f
	v_readlane_b32 s38, v250, 34
	v_readlane_b32 s39, v250, 35
	v_readlane_b32 s40, v250, 36
	v_readlane_b32 s41, v250, 37
	v_readlane_b32 s15, v250, 55
	s_add_u32 s28, s78, 0x8500000
	s_addc_u32 s29, s79, 0
	s_mov_b32 s16, 0x4b3fff81
	s_mov_b32 s17, 0x0c0c0400
	s_mov_b32 s26, 0x04000c0c
	s_cmp_lt_u32 s12, s14
	s_cbranch_scc0 .Lq_done
	s_cmp_ge_u32 s12, 0x7000
	s_cselect_b32 s31, 0x7000, 0
	s_cselect_b32 s33, 0x40000, 0
	s_cselect_b32 s6, s40, s38
	s_cselect_b32 s7, s41, s39
	s_sub_u32 s30, s12, s31
	s_lshr_b32 s34, s30, 9
	s_mul_i32 s34, s34, 0x2493
	s_lshr_b32 s34, s34, 16
	s_mul_i32 s35, s34, 0xe00
	s_sub_u32 s30, s30, s35
	s_lshr_b32 s35, s30, 5
	s_mul_i32 s35, s35, 0x2493
	s_lshr_b32 s35, s35, 16
	s_mul_i32 s36, s35, 224
	s_sub_u32 s30, s30, s36
	s_mul_i32 s36, s34, 0x3800000
	s_mul_i32 s37, s35, 0x380000
	s_add_u32 s36, s36, s37
	s_lshl_b32 s37, s30, 7
	s_add_u32 s36, s36, s37
	s_add_u32 s6, s6, s36
	s_addc_u32 s7, s7, 0
	s_mul_i32 s36, s34, 0x1c00000
	s_add_u32 s36, s36, s33
	s_lshr_b32 s37, s30, 2
	s_lshl_b32 s37, s37, 19
	s_add_u32 s36, s36, s37
	s_and_b32 s37, s30, 3
	s_lshl_b32 s37, s37, 16
	s_add_u32 s36, s36, s37
	s_lshl_b32 s37, s35, 7
	s_add_u32 s36, s36, s37
	s_add_u32 s8, s28, s36
	s_addc_u32 s9, s29, 0
	global_load_dwordx4 v[2:5], v130, s[6:7]
	global_load_dwordx4 v[6:9], v131, s[6:7]
	global_load_dwordx4 v[10:13], v132, s[6:7]
	global_load_dwordx4 v[14:17], v133, s[6:7]
	global_load_dwordx4 v[18:21], v134, s[6:7]
	global_load_dwordx4 v[22:25], v135, s[6:7]
	global_load_dwordx4 v[26:29], v136, s[6:7]
	global_load_dwordx4 v[30:33], v137, s[6:7]
	global_load_dwordx4 v[34:37], v138, s[6:7]
	global_load_dwordx4 v[38:41], v139, s[6:7]
	global_load_dwordx4 v[42:45], v140, s[6:7]
	global_load_dwordx4 v[46:49], v141, s[6:7]
	global_load_dwordx4 v[50:53], v142, s[6:7]
	global_load_dwordx4 v[54:57], v143, s[6:7]
	global_load_dwordx4 v[58:61], v144, s[6:7]
	global_load_dwordx4 v[62:65], v145, s[6:7]
	s_add_u32 s12, s12, s13
	s_cmp_lt_u32 s12, s14
	s_cbranch_scc0 .Lq_tailA
	s_cmp_ge_u32 s12, 0x7000
	s_cselect_b32 s31, 0x7000, 0
	s_cselect_b32 s33, 0x40000, 0
	s_cselect_b32 s6, s40, s38
	s_cselect_b32 s7, s41, s39
	s_sub_u32 s30, s12, s31
	s_lshr_b32 s34, s30, 9
	s_mul_i32 s34, s34, 0x2493
	s_lshr_b32 s34, s34, 16
	s_mul_i32 s35, s34, 0xe00
	s_sub_u32 s30, s30, s35
	s_lshr_b32 s35, s30, 5
	s_mul_i32 s35, s35, 0x2493
	s_lshr_b32 s35, s35, 16
	s_mul_i32 s36, s35, 224
	s_sub_u32 s30, s30, s36
	s_mul_i32 s36, s34, 0x3800000
	s_mul_i32 s37, s35, 0x380000
	s_add_u32 s36, s36, s37
	s_lshl_b32 s37, s30, 7
	s_add_u32 s36, s36, s37
	s_add_u32 s6, s6, s36
	s_addc_u32 s7, s7, 0
	s_mul_i32 s36, s34, 0x1c00000
	s_add_u32 s36, s36, s33
	s_lshr_b32 s37, s30, 2
	s_lshl_b32 s37, s37, 19
	s_add_u32 s36, s36, s37
	s_and_b32 s37, s30, 3
	s_lshl_b32 s37, s37, 16
	s_add_u32 s36, s36, s37
	s_lshl_b32 s37, s35, 7
	s_add_u32 s36, s36, s37
	s_add_u32 s10, s28, s36
	s_addc_u32 s11, s29, 0
	global_load_dwordx4 v[66:69], v130, s[6:7]
	global_load_dwordx4 v[70:73], v131, s[6:7]
	global_load_dwordx4 v[74:77], v132, s[6:7]
	global_load_dwordx4 v[78:81], v133, s[6:7]
	global_load_dwordx4 v[82:85], v134, s[6:7]
	global_load_dwordx4 v[86:89], v135, s[6:7]
	global_load_dwordx4 v[90:93], v136, s[6:7]
	global_load_dwordx4 v[94:97], v137, s[6:7]
	global_load_dwordx4 v[98:101], v138, s[6:7]
	global_load_dwordx4 v[102:105], v139, s[6:7]
	global_load_dwordx4 v[106:109], v140, s[6:7]
	global_load_dwordx4 v[110:113], v141, s[6:7]
	global_load_dwordx4 v[114:117], v142, s[6:7]
	global_load_dwordx4 v[118:121], v143, s[6:7]
	global_load_dwordx4 v[122:125], v144, s[6:7]
	global_load_dwordx4 v[126:129], v145, s[6:7]
	s_waitcnt vmcnt(16)
	v_fma_f32 v168, v2, s15, v166
	v_fma_f32 v169, v6, s15, v166
	v_fma_f32 v170, v10, s15, v166
	v_fma_f32 v171, v14, s15, v166
	v_med3_f32 v168, v168, s16, v167
	v_med3_f32 v169, v169, s16, v167
	v_med3_f32 v170, v170, s16, v167
	v_med3_f32 v171, v171, s16, v167
	v_perm_b32 v168, v169, v168, s17
	v_perm_b32 v170, v171, v170, s26
	v_or_b32_e32 v150, v170, v168
	v_fma_f32 v168, v18, s15, v166
	v_fma_f32 v169, v22, s15, v166
	v_fma_f32 v170, v26, s15, v166
	v_fma_f32 v171, v30, s15, v166
	v_med3_f32 v168, v168, s16, v167
	v_med3_f32 v169, v169, s16, v167
	v_med3_f32 v170, v170, s16, v167
	v_med3_f32 v171, v171, s16, v167
	v_perm_b32 v168, v169, v168, s17
	v_perm_b32 v170, v171, v170, s26
	v_or_b32_e32 v151, v170, v168
	v_fma_f32 v168, v34, s15, v166
	v_fma_f32 v169, v38, s15, v166
	v_fma_f32 v170, v42, s15, v166
	v_fma_f32 v171, v46, s15, v166
	v_med3_f32 v168, v168, s16, v167
	v_med3_f32 v169, v169, s16, v167
	v_med3_f32 v170, v170, s16, v167
	v_med3_f32 v171, v171, s16, v167
	v_perm_b32 v168, v169, v168, s17
	v_perm_b32 v170, v171, v170, s26
	v_or_b32_e32 v152, v170, v168
	v_fma_f32 v168, v50, s15, v166
	v_fma_f32 v169, v54, s15, v166
	v_fma_f32 v170, v58, s15, v166
	v_fma_f32 v171, v62, s15, v166
	v_med3_f32 v168, v168, s16, v167
	v_med3_f32 v169, v169, s16, v167
	v_med3_f32 v170, v170, s16, v167
	v_med3_f32 v171, v171, s16, v167
	v_perm_b32 v168, v169, v168, s17
	v_perm_b32 v170, v171, v170, s26
	v_or_b32_e32 v153, v170, v168
	v_fma_f32 v168, v3, s15, v166
	v_fma_f32 v169, v7, s15, v166
	v_fma_f32 v170, v11, s15, v166
	v_fma_f32 v171, v15, s15, v166
	v_med3_f32 v168, v168, s16, v167
	v_med3_f32 v169, v169, s16, v167
	v_med3_f32 v170, v170, s16, v167
	v_med3_f32 v171, v171, s16, v167
	v_perm_b32 v168, v169, v168, s17
	v_perm_b32 v170, v171, v170, s26
	v_or_b32_e32 v154, v170, v168
	v_fma_f32 v168, v19, s15, v166
	v_fma_f32 v169, v23, s15, v166
	v_fma_f32 v170, v27, s15, v166
	v_fma_f32 v171, v31, s15, v166
	v_med3_f32 v168, v168, s16, v167
	v_med3_f32 v169, v169, s16, v167
	v_med3_f32 v170, v170, s16, v167
	v_med3_f32 v171, v171, s16, v167
	v_perm_b32 v168, v169, v168, s17
	v_perm_b32 v170, v171, v170, s26
	v_or_b32_e32 v155, v170, v168
	v_fma_f32 v168, v35, s15, v166
	v_fma_f32 v169, v39, s15, v166
	v_fma_f32 v170, v43, s15, v166
	v_fma_f32 v171, v47, s15, v166
	v_med3_f32 v168, v168, s16, v167
	v_med3_f32 v169, v169, s16, v167
	v_med3_f32 v170, v170, s16, v167
	v_med3_f32 v171, v171, s16, v167
	v_perm_b32 v168, v169, v168, s17
	v_perm_b32 v170, v171, v170, s26
	v_or_b32_e32 v156, v170, v168
	v_fma_f32 v168, v51, s15, v166
	v_fma_f32 v169, v55, s15, v166
	v_fma_f32 v170, v59, s15, v166
	v_fma_f32 v171, v63, s15, v166
	v_med3_f32 v168, v168, s16, v167
	v_med3_f32 v169, v169, s16, v167
	v_med3_f32 v170, v170, s16, v167
	v_med3_f32 v171, v171, s16, v167
	v_perm_b32 v168, v169, v168, s17
	v_perm_b32 v170, v171, v170, s26
	v_or_b32_e32 v157, v170, v168
	v_fma_f32 v168, v4, s15, v166
	v_fma_f32 v169, v8, s15, v166
	v_fma_f32 v170, v12, s15, v166
	v_fma_f32 v171, v16, s15, v166
	v_med3_f32 v168, v168, s16, v167
	v_med3_f32 v169, v169, s16, v167
	v_med3_f32 v170, v170, s16, v167
	v_med3_f32 v171, v171, s16, v167
	v_perm_b32 v168, v169, v168, s17
	v_perm_b32 v170, v171, v170, s26
	v_or_b32_e32 v158, v170, v168
	v_fma_f32 v168, v20, s15, v166
	v_fma_f32 v169, v24, s15, v166
	v_fma_f32 v170, v28, s15, v166
	v_fma_f32 v171, v32, s15, v166
	v_med3_f32 v168, v168, s16, v167
	v_med3_f32 v169, v169, s16, v167
	v_med3_f32 v170, v170, s16, v167
	v_med3_f32 v171, v171, s16, v167
	v_perm_b32 v168, v169, v168, s17
	v_perm_b32 v170, v171, v170, s26
	v_or_b32_e32 v159, v170, v168
	v_fma_f32 v168, v36, s15, v166
	v_fma_f32 v169, v40, s15, v166
	v_fma_f32 v170, v44, s15, v166
	v_fma_f32 v171, v48, s15, v166
	v_med3_f32 v168, v168, s16, v167
	v_med3_f32 v169, v169, s16, v167
	v_med3_f32 v170, v170, s16, v167
	v_med3_f32 v171, v171, s16, v167
	v_perm_b32 v168, v169, v168, s17
	v_perm_b32 v170, v171, v170, s26
	v_or_b32_e32 v160, v170, v168
	v_fma_f32 v168, v52, s15, v166
	v_fma_f32 v169, v56, s15, v166
	v_fma_f32 v170, v60, s15, v166
	v_fma_f32 v171, v64, s15, v166
	v_med3_f32 v168, v168, s16, v167
	v_med3_f32 v169, v169, s16, v167
	v_med3_f32 v170, v170, s16, v167
	v_med3_f32 v171, v171, s16, v167
	v_perm_b32 v168, v169, v168, s17
	v_perm_b32 v170, v171, v170, s26
	v_or_b32_e32 v161, v170, v168
	v_fma_f32 v168, v5, s15, v166
	v_fma_f32 v169, v9, s15, v166
	v_fma_f32 v170, v13, s15, v166
	v_fma_f32 v171, v17, s15, v166
	v_med3_f32 v168, v168, s16, v167
	v_med3_f32 v169, v169, s16, v167
	v_med3_f32 v170, v170, s16, v167
	v_med3_f32 v171, v171, s16, v167
	v_perm_b32 v168, v169, v168, s17
	v_perm_b32 v170, v171, v170, s26
	v_or_b32_e32 v162, v170, v168
	v_fma_f32 v168, v21, s15, v166
	v_fma_f32 v169, v25, s15, v166
	v_fma_f32 v170, v29, s15, v166
	v_fma_f32 v171, v33, s15, v166
	v_med3_f32 v168, v168, s16, v167
	v_med3_f32 v169, v169, s16, v167
	v_med3_f32 v170, v170, s16, v167
	v_med3_f32 v171, v171, s16, v167
	v_perm_b32 v168, v169, v168, s17
	v_perm_b32 v170, v171, v170, s26
	v_or_b32_e32 v163, v170, v168
	v_fma_f32 v168, v37, s15, v166
	v_fma_f32 v169, v41, s15, v166
	v_fma_f32 v170, v45, s15, v166
	v_fma_f32 v171, v49, s15, v166
	v_med3_f32 v168, v168, s16, v167
	v_med3_f32 v169, v169, s16, v167
	v_med3_f32 v170, v170, s16, v167
	v_med3_f32 v171, v171, s16, v167
	v_perm_b32 v168, v169, v168, s17
	v_perm_b32 v170, v171, v170, s26
	v_or_b32_e32 v164, v170, v168
	v_fma_f32 v168, v53, s15, v166
	v_fma_f32 v169, v57, s15, v166
	v_fma_f32 v170, v61, s15, v166
	v_fma_f32 v171, v65, s15, v166
	v_med3_f32 v168, v168, s16, v167
	v_med3_f32 v169, v169, s16, v167
	v_med3_f32 v170, v170, s16, v167
	v_med3_f32 v171, v171, s16, v167
	v_perm_b32 v168, v169, v168, s17
	v_perm_b32 v170, v171, v170, s26
	v_or_b32_e32 v165, v170, v168
	global_store_dwordx4 v146, v[150:153], s[8:9]
	global_store_dwordx4 v147, v[154:157], s[8:9]
	global_store_dwordx4 v148, v[158:161], s[8:9]
	global_store_dwordx4 v149, v[162:165], s[8:9]
.Lq_loop:
	s_add_u32 s12, s12, s13
	s_cmp_lt_u32 s12, s14
	s_cbranch_scc0 .Lq_tailB
	s_cmp_ge_u32 s12, 0x7000
	s_cselect_b32 s31, 0x7000, 0
	s_cselect_b32 s33, 0x40000, 0
	s_cselect_b32 s6, s40, s38
	s_cselect_b32 s7, s41, s39
	s_sub_u32 s30, s12, s31
	s_lshr_b32 s34, s30, 9
	s_mul_i32 s34, s34, 0x2493
	s_lshr_b32 s34, s34, 16
	s_mul_i32 s35, s34, 0xe00
	s_sub_u32 s30, s30, s35
	s_lshr_b32 s35, s30, 5
	s_mul_i32 s35, s35, 0x2493
	s_lshr_b32 s35, s35, 16
	s_mul_i32 s36, s35, 224
	s_sub_u32 s30, s30, s36
	s_mul_i32 s36, s34, 0x3800000
	s_mul_i32 s37, s35, 0x380000
	s_add_u32 s36, s36, s37
	s_lshl_b32 s37, s30, 7
	s_add_u32 s36, s36, s37
	s_add_u32 s6, s6, s36
	s_addc_u32 s7, s7, 0
	s_mul_i32 s36, s34, 0x1c00000
	s_add_u32 s36, s36, s33
	s_lshr_b32 s37, s30, 2
	s_lshl_b32 s37, s37, 19
	s_add_u32 s36, s36, s37
	s_and_b32 s37, s30, 3
	s_lshl_b32 s37, s37, 16
	s_add_u32 s36, s36, s37
	s_lshl_b32 s37, s35, 7
	s_add_u32 s36, s36, s37
	s_add_u32 s8, s28, s36
	s_addc_u32 s9, s29, 0
	global_load_dwordx4 v[2:5], v130, s[6:7]
	global_load_dwordx4 v[6:9], v131, s[6:7]
	global_load_dwordx4 v[10:13], v132, s[6:7]
	global_load_dwordx4 v[14:17], v133, s[6:7]
	global_load_dwordx4 v[18:21], v134, s[6:7]
	global_load_dwordx4 v[22:25], v135, s[6:7]
	global_load_dwordx4 v[26:29], v136, s[6:7]
	global_load_dwordx4 v[30:33], v137, s[6:7]
	global_load_dwordx4 v[34:37], v138, s[6:7]
	global_load_dwordx4 v[38:41], v139, s[6:7]
	global_load_dwordx4 v[42:45], v140, s[6:7]
	global_load_dwordx4 v[46:49], v141, s[6:7]
	global_load_dwordx4 v[50:53], v142, s[6:7]
	global_load_dwordx4 v[54:57], v143, s[6:7]
	global_load_dwordx4 v[58:61], v144, s[6:7]
	global_load_dwordx4 v[62:65], v145, s[6:7]
	s_waitcnt vmcnt(20)
	v_fma_f32 v168, v66, s15, v166
	v_fma_f32 v169, v70, s15, v166
	v_fma_f32 v170, v74, s15, v166
	v_fma_f32 v171, v78, s15, v166
	v_med3_f32 v168, v168, s16, v167
	v_med3_f32 v169, v169, s16, v167
	v_med3_f32 v170, v170, s16, v167
	v_med3_f32 v171, v171, s16, v167
	v_perm_b32 v168, v169, v168, s17
	v_perm_b32 v170, v171, v170, s26
	v_or_b32_e32 v150, v170, v168
	v_fma_f32 v168, v82, s15, v166
	v_fma_f32 v169, v86, s15, v166
	v_fma_f32 v170, v90, s15, v166
	v_fma_f32 v171, v94, s15, v166
	v_med3_f32 v168, v168, s16, v167
	v_med3_f32 v169, v169, s16, v167
	v_med3_f32 v170, v170, s16, v167
	v_med3_f32 v171, v171, s16, v167
	v_perm_b32 v168, v169, v168, s17
	v_perm_b32 v170, v171, v170, s26
	v_or_b32_e32 v151, v170, v168
	v_fma_f32 v168, v98, s15, v166
	v_fma_f32 v169, v102, s15, v166
	v_fma_f32 v170, v106, s15, v166
	v_fma_f32 v171, v110, s15, v166
	v_med3_f32 v168, v168, s16, v167
	v_med3_f32 v169, v169, s16, v167
	v_med3_f32 v170, v170, s16, v167
	v_med3_f32 v171, v171, s16, v167
	v_perm_b32 v168, v169, v168, s17
	v_perm_b32 v170, v171, v170, s26
	v_or_b32_e32 v152, v170, v168
	v_fma_f32 v168, v114, s15, v166
	v_fma_f32 v169, v118, s15, v166
	v_fma_f32 v170, v122, s15, v166
	v_fma_f32 v171, v126, s15, v166
	v_med3_f32 v168, v168, s16, v167
	v_med3_f32 v169, v169, s16, v167
	v_med3_f32 v170, v170, s16, v167
	v_med3_f32 v171, v171, s16, v167
	v_perm_b32 v168, v169, v168, s17
	v_perm_b32 v170, v171, v170, s26
	v_or_b32_e32 v153, v170, v168
	v_fma_f32 v168, v67, s15, v166
	v_fma_f32 v169, v71, s15, v166
	v_fma_f32 v170, v75, s15, v166
	v_fma_f32 v171, v79, s15, v166
	v_med3_f32 v168, v168, s16, v167
	v_med3_f32 v169, v169, s16, v167
	v_med3_f32 v170, v170, s16, v167
	v_med3_f32 v171, v171, s16, v167
	v_perm_b32 v168, v169, v168, s17
	v_perm_b32 v170, v171, v170, s26
	v_or_b32_e32 v154, v170, v168
	v_fma_f32 v168, v83, s15, v166
	v_fma_f32 v169, v87, s15, v166
	v_fma_f32 v170, v91, s15, v166
	v_fma_f32 v171, v95, s15, v166
	v_med3_f32 v168, v168, s16, v167
	v_med3_f32 v169, v169, s16, v167
	v_med3_f32 v170, v170, s16, v167
	v_med3_f32 v171, v171, s16, v167
	v_perm_b32 v168, v169, v168, s17
	v_perm_b32 v170, v171, v170, s26
	v_or_b32_e32 v155, v170, v168
	v_fma_f32 v168, v99, s15, v166
	v_fma_f32 v169, v103, s15, v166
	v_fma_f32 v170, v107, s15, v166
	v_fma_f32 v171, v111, s15, v166
	v_med3_f32 v168, v168, s16, v167
	v_med3_f32 v169, v169, s16, v167
	v_med3_f32 v170, v170, s16, v167
	v_med3_f32 v171, v171, s16, v167
	v_perm_b32 v168, v169, v168, s17
	v_perm_b32 v170, v171, v170, s26
	v_or_b32_e32 v156, v170, v168
	v_fma_f32 v168, v115, s15, v166
	v_fma_f32 v169, v119, s15, v166
	v_fma_f32 v170, v123, s15, v166
	v_fma_f32 v171, v127, s15, v166
	v_med3_f32 v168, v168, s16, v167
	v_med3_f32 v169, v169, s16, v167
	v_med3_f32 v170, v170, s16, v167
	v_med3_f32 v171, v171, s16, v167
	v_perm_b32 v168, v169, v168, s17
	v_perm_b32 v170, v171, v170, s26
	v_or_b32_e32 v157, v170, v168
	v_fma_f32 v168, v68, s15, v166
	v_fma_f32 v169, v72, s15, v166
	v_fma_f32 v170, v76, s15, v166
	v_fma_f32 v171, v80, s15, v166
	v_med3_f32 v168, v168, s16, v167
	v_med3_f32 v169, v169, s16, v167
	v_med3_f32 v170, v170, s16, v167
	v_med3_f32 v171, v171, s16, v167
	v_perm_b32 v168, v169, v168, s17
	v_perm_b32 v170, v171, v170, s26
	v_or_b32_e32 v158, v170, v168
	v_fma_f32 v168, v84, s15, v166
	v_fma_f32 v169, v88, s15, v166
	v_fma_f32 v170, v92, s15, v166
	v_fma_f32 v171, v96, s15, v166
	v_med3_f32 v168, v168, s16, v167
	v_med3_f32 v169, v169, s16, v167
	v_med3_f32 v170, v170, s16, v167
	v_med3_f32 v171, v171, s16, v167
	v_perm_b32 v168, v169, v168, s17
	v_perm_b32 v170, v171, v170, s26
	v_or_b32_e32 v159, v170, v168
	v_fma_f32 v168, v100, s15, v166
	v_fma_f32 v169, v104, s15, v166
	v_fma_f32 v170, v108, s15, v166
	v_fma_f32 v171, v112, s15, v166
	v_med3_f32 v168, v168, s16, v167
	v_med3_f32 v169, v169, s16, v167
	v_med3_f32 v170, v170, s16, v167
	v_med3_f32 v171, v171, s16, v167
	v_perm_b32 v168, v169, v168, s17
	v_perm_b32 v170, v171, v170, s26
	v_or_b32_e32 v160, v170, v168
	v_fma_f32 v168, v116, s15, v166
	v_fma_f32 v169, v120, s15, v166
	v_fma_f32 v170, v124, s15, v166
	v_fma_f32 v171, v128, s15, v166
	v_med3_f32 v168, v168, s16, v167
	v_med3_f32 v169, v169, s16, v167
	v_med3_f32 v170, v170, s16, v167
	v_med3_f32 v171, v171, s16, v167
	v_perm_b32 v168, v169, v168, s17
	v_perm_b32 v170, v171, v170, s26
	v_or_b32_e32 v161, v170, v168
	v_fma_f32 v168, v69, s15, v166
	v_fma_f32 v169, v73, s15, v166
	v_fma_f32 v170, v77, s15, v166
	v_fma_f32 v171, v81, s15, v166
	v_med3_f32 v168, v168, s16, v167
	v_med3_f32 v169, v169, s16, v167
	v_med3_f32 v170, v170, s16, v167
	v_med3_f32 v171, v171, s16, v167
	v_perm_b32 v168, v169, v168, s17
	v_perm_b32 v170, v171, v170, s26
	v_or_b32_e32 v162, v170, v168
	v_fma_f32 v168, v85, s15, v166
	v_fma_f32 v169, v89, s15, v166
	v_fma_f32 v170, v93, s15, v166
	v_fma_f32 v171, v97, s15, v166
	v_med3_f32 v168, v168, s16, v167
	v_med3_f32 v169, v169, s16, v167
	v_med3_f32 v170, v170, s16, v167
	v_med3_f32 v171, v171, s16, v167
	v_perm_b32 v168, v169, v168, s17
	v_perm_b32 v170, v171, v170, s26
	v_or_b32_e32 v163, v170, v168
	v_fma_f32 v168, v101, s15, v166
	v_fma_f32 v169, v105, s15, v166
	v_fma_f32 v170, v109, s15, v166
	v_fma_f32 v171, v113, s15, v166
	v_med3_f32 v168, v168, s16, v167
	v_med3_f32 v169, v169, s16, v167
	v_med3_f32 v170, v170, s16, v167
	v_med3_f32 v171, v171, s16, v167
	v_perm_b32 v168, v169, v168, s17
	v_perm_b32 v170, v171, v170, s26
	v_or_b32_e32 v164, v170, v168
	v_fma_f32 v168, v117, s15, v166
	v_fma_f32 v169, v121, s15, v166
	v_fma_f32 v170, v125, s15, v166
	v_fma_f32 v171, v129, s15, v166
	v_med3_f32 v168, v168, s16, v167
	v_med3_f32 v169, v169, s16, v167
	v_med3_f32 v170, v170, s16, v167
	v_med3_f32 v171, v171, s16, v167
	v_perm_b32 v168, v169, v168, s17
	v_perm_b32 v170, v171, v170, s26
	v_or_b32_e32 v165, v170, v168
	global_store_dwordx4 v146, v[150:153], s[10:11]
	global_store_dwordx4 v147, v[154:157], s[10:11]
	global_store_dwordx4 v148, v[158:161], s[10:11]
	global_store_dwordx4 v149, v[162:165], s[10:11]
	s_add_u32 s12, s12, s13
	s_cmp_lt_u32 s12, s14
	s_cbranch_scc0 .Lq_tailA
	s_cmp_ge_u32 s12, 0x7000
	s_cselect_b32 s31, 0x7000, 0
	s_cselect_b32 s33, 0x40000, 0
	s_cselect_b32 s6, s40, s38
	s_cselect_b32 s7, s41, s39
	s_sub_u32 s30, s12, s31
	s_lshr_b32 s34, s30, 9
	s_mul_i32 s34, s34, 0x2493
	s_lshr_b32 s34, s34, 16
	s_mul_i32 s35, s34, 0xe00
	s_sub_u32 s30, s30, s35
	s_lshr_b32 s35, s30, 5
	s_mul_i32 s35, s35, 0x2493
	s_lshr_b32 s35, s35, 16
	s_mul_i32 s36, s35, 224
	s_sub_u32 s30, s30, s36
	s_mul_i32 s36, s34, 0x3800000
	s_mul_i32 s37, s35, 0x380000
	s_add_u32 s36, s36, s37
	s_lshl_b32 s37, s30, 7
	s_add_u32 s36, s36, s37
	s_add_u32 s6, s6, s36
	s_addc_u32 s7, s7, 0
	s_mul_i32 s36, s34, 0x1c00000
	s_add_u32 s36, s36, s33
	s_lshr_b32 s37, s30, 2
	s_lshl_b32 s37, s37, 19
	s_add_u32 s36, s36, s37
	s_and_b32 s37, s30, 3
	s_lshl_b32 s37, s37, 16
	s_add_u32 s36, s36, s37
	s_lshl_b32 s37, s35, 7
	s_add_u32 s36, s36, s37
	s_add_u32 s10, s28, s36
	s_addc_u32 s11, s29, 0
	global_load_dwordx4 v[66:69], v130, s[6:7]
	global_load_dwordx4 v[70:73], v131, s[6:7]
	global_load_dwordx4 v[74:77], v132, s[6:7]
	global_load_dwordx4 v[78:81], v133, s[6:7]
	global_load_dwordx4 v[82:85], v134, s[6:7]
	global_load_dwordx4 v[86:89], v135, s[6:7]
	global_load_dwordx4 v[90:93], v136, s[6:7]
	global_load_dwordx4 v[94:97], v137, s[6:7]
	global_load_dwordx4 v[98:101], v138, s[6:7]
	global_load_dwordx4 v[102:105], v139, s[6:7]
	global_load_dwordx4 v[106:109], v140, s[6:7]
	global_load_dwordx4 v[110:113], v141, s[6:7]
	global_load_dwordx4 v[114:117], v142, s[6:7]
	global_load_dwordx4 v[118:121], v143, s[6:7]
	global_load_dwordx4 v[122:125], v144, s[6:7]
	global_load_dwordx4 v[126:129], v145, s[6:7]
	s_waitcnt vmcnt(20)
	v_fma_f32 v168, v2, s15, v166
	v_fma_f32 v169, v6, s15, v166
	v_fma_f32 v170, v10, s15, v166
	v_fma_f32 v171, v14, s15, v166
	v_med3_f32 v168, v168, s16, v167
	v_med3_f32 v169, v169, s16, v167
	v_med3_f32 v170, v170, s16, v167
	v_med3_f32 v171, v171, s16, v167
	v_perm_b32 v168, v169, v168, s17
	v_perm_b32 v170, v171, v170, s26
	v_or_b32_e32 v150, v170, v168
	v_fma_f32 v168, v18, s15, v166
	v_fma_f32 v169, v22, s15, v166
	v_fma_f32 v170, v26, s15, v166
	v_fma_f32 v171, v30, s15, v166
	v_med3_f32 v168, v168, s16, v167
	v_med3_f32 v169, v169, s16, v167
	v_med3_f32 v170, v170, s16, v167
	v_med3_f32 v171, v171, s16, v167
	v_perm_b32 v168, v169, v168, s17
	v_perm_b32 v170, v171, v170, s26
	v_or_b32_e32 v151, v170, v168
	v_fma_f32 v168, v34, s15, v166
	v_fma_f32 v169, v38, s15, v166
	v_fma_f32 v170, v42, s15, v166
	v_fma_f32 v171, v46, s15, v166
	v_med3_f32 v168, v168, s16, v167
	v_med3_f32 v169, v169, s16, v167
	v_med3_f32 v170, v170, s16, v167
	v_med3_f32 v171, v171, s16, v167
	v_perm_b32 v168, v169, v168, s17
	v_perm_b32 v170, v171, v170, s26
	v_or_b32_e32 v152, v170, v168
	v_fma_f32 v168, v50, s15, v166
	v_fma_f32 v169, v54, s15, v166
	v_fma_f32 v170, v58, s15, v166
	v_fma_f32 v171, v62, s15, v166
	v_med3_f32 v168, v168, s16, v167
	v_med3_f32 v169, v169, s16, v167
	v_med3_f32 v170, v170, s16, v167
	v_med3_f32 v171, v171, s16, v167
	v_perm_b32 v168, v169, v168, s17
	v_perm_b32 v170, v171, v170, s26
	v_or_b32_e32 v153, v170, v168
	v_fma_f32 v168, v3, s15, v166
	v_fma_f32 v169, v7, s15, v166
	v_fma_f32 v170, v11, s15, v166
	v_fma_f32 v171, v15, s15, v166
	v_med3_f32 v168, v168, s16, v167
	v_med3_f32 v169, v169, s16, v167
	v_med3_f32 v170, v170, s16, v167
	v_med3_f32 v171, v171, s16, v167
	v_perm_b32 v168, v169, v168, s17
	v_perm_b32 v170, v171, v170, s26
	v_or_b32_e32 v154, v170, v168
	v_fma_f32 v168, v19, s15, v166
	v_fma_f32 v169, v23, s15, v166
	v_fma_f32 v170, v27, s15, v166
	v_fma_f32 v171, v31, s15, v166
	v_med3_f32 v168, v168, s16, v167
	v_med3_f32 v169, v169, s16, v167
	v_med3_f32 v170, v170, s16, v167
	v_med3_f32 v171, v171, s16, v167
	v_perm_b32 v168, v169, v168, s17
	v_perm_b32 v170, v171, v170, s26
	v_or_b32_e32 v155, v170, v168
	v_fma_f32 v168, v35, s15, v166
	v_fma_f32 v169, v39, s15, v166
	v_fma_f32 v170, v43, s15, v166
	v_fma_f32 v171, v47, s15, v166
	v_med3_f32 v168, v168, s16, v167
	v_med3_f32 v169, v169, s16, v167
	v_med3_f32 v170, v170, s16, v167
	v_med3_f32 v171, v171, s16, v167
	v_perm_b32 v168, v169, v168, s17
	v_perm_b32 v170, v171, v170, s26
	v_or_b32_e32 v156, v170, v168
	v_fma_f32 v168, v51, s15, v166
	v_fma_f32 v169, v55, s15, v166
	v_fma_f32 v170, v59, s15, v166
	v_fma_f32 v171, v63, s15, v166
	v_med3_f32 v168, v168, s16, v167
	v_med3_f32 v169, v169, s16, v167
	v_med3_f32 v170, v170, s16, v167
	v_med3_f32 v171, v171, s16, v167
	v_perm_b32 v168, v169, v168, s17
	v_perm_b32 v170, v171, v170, s26
	v_or_b32_e32 v157, v170, v168
	v_fma_f32 v168, v4, s15, v166
	v_fma_f32 v169, v8, s15, v166
	v_fma_f32 v170, v12, s15, v166
	v_fma_f32 v171, v16, s15, v166
	v_med3_f32 v168, v168, s16, v167
	v_med3_f32 v169, v169, s16, v167
	v_med3_f32 v170, v170, s16, v167
	v_med3_f32 v171, v171, s16, v167
	v_perm_b32 v168, v169, v168, s17
	v_perm_b32 v170, v171, v170, s26
	v_or_b32_e32 v158, v170, v168
	v_fma_f32 v168, v20, s15, v166
	v_fma_f32 v169, v24, s15, v166
	v_fma_f32 v170, v28, s15, v166
	v_fma_f32 v171, v32, s15, v166
	v_med3_f32 v168, v168, s16, v167
	v_med3_f32 v169, v169, s16, v167
	v_med3_f32 v170, v170, s16, v167
	v_med3_f32 v171, v171, s16, v167
	v_perm_b32 v168, v169, v168, s17
	v_perm_b32 v170, v171, v170, s26
	v_or_b32_e32 v159, v170, v168
	v_fma_f32 v168, v36, s15, v166
	v_fma_f32 v169, v40, s15, v166
	v_fma_f32 v170, v44, s15, v166
	v_fma_f32 v171, v48, s15, v166
	v_med3_f32 v168, v168, s16, v167
	v_med3_f32 v169, v169, s16, v167
	v_med3_f32 v170, v170, s16, v167
	v_med3_f32 v171, v171, s16, v167
	v_perm_b32 v168, v169, v168, s17
	v_perm_b32 v170, v171, v170, s26
	v_or_b32_e32 v160, v170, v168
	v_fma_f32 v168, v52, s15, v166
	v_fma_f32 v169, v56, s15, v166
	v_fma_f32 v170, v60, s15, v166
	v_fma_f32 v171, v64, s15, v166
	v_med3_f32 v168, v168, s16, v167
	v_med3_f32 v169, v169, s16, v167
	v_med3_f32 v170, v170, s16, v167
	v_med3_f32 v171, v171, s16, v167
	v_perm_b32 v168, v169, v168, s17
	v_perm_b32 v170, v171, v170, s26
	v_or_b32_e32 v161, v170, v168
	v_fma_f32 v168, v5, s15, v166
	v_fma_f32 v169, v9, s15, v166
	v_fma_f32 v170, v13, s15, v166
	v_fma_f32 v171, v17, s15, v166
	v_med3_f32 v168, v168, s16, v167
	v_med3_f32 v169, v169, s16, v167
	v_med3_f32 v170, v170, s16, v167
	v_med3_f32 v171, v171, s16, v167
	v_perm_b32 v168, v169, v168, s17
	v_perm_b32 v170, v171, v170, s26
	v_or_b32_e32 v162, v170, v168
	v_fma_f32 v168, v21, s15, v166
	v_fma_f32 v169, v25, s15, v166
	v_fma_f32 v170, v29, s15, v166
	v_fma_f32 v171, v33, s15, v166
	v_med3_f32 v168, v168, s16, v167
	v_med3_f32 v169, v169, s16, v167
	v_med3_f32 v170, v170, s16, v167
	v_med3_f32 v171, v171, s16, v167
	v_perm_b32 v168, v169, v168, s17
	v_perm_b32 v170, v171, v170, s26
	v_or_b32_e32 v163, v170, v168
	v_fma_f32 v168, v37, s15, v166
	v_fma_f32 v169, v41, s15, v166
	v_fma_f32 v170, v45, s15, v166
	v_fma_f32 v171, v49, s15, v166
	v_med3_f32 v168, v168, s16, v167
	v_med3_f32 v169, v169, s16, v167
	v_med3_f32 v170, v170, s16, v167
	v_med3_f32 v171, v171, s16, v167
	v_perm_b32 v168, v169, v168, s17
	v_perm_b32 v170, v171, v170, s26
	v_or_b32_e32 v164, v170, v168
	v_fma_f32 v168, v53, s15, v166
	v_fma_f32 v169, v57, s15, v166
	v_fma_f32 v170, v61, s15, v166
	v_fma_f32 v171, v65, s15, v166
	v_med3_f32 v168, v168, s16, v167
	v_med3_f32 v169, v169, s16, v167
	v_med3_f32 v170, v170, s16, v167
	v_med3_f32 v171, v171, s16, v167
	v_perm_b32 v168, v169, v168, s17
	v_perm_b32 v170, v171, v170, s26
	v_or_b32_e32 v165, v170, v168
	global_store_dwordx4 v146, v[150:153], s[8:9]
	global_store_dwordx4 v147, v[154:157], s[8:9]
	global_store_dwordx4 v148, v[158:161], s[8:9]
	global_store_dwordx4 v149, v[162:165], s[8:9]
	s_branch .Lq_loop
.Lq_tailB:
	s_waitcnt vmcnt(0)
	v_fma_f32 v168, v66, s15, v166
	v_fma_f32 v169, v70, s15, v166
	v_fma_f32 v170, v74, s15, v166
	v_fma_f32 v171, v78, s15, v166
	v_med3_f32 v168, v168, s16, v167
	v_med3_f32 v169, v169, s16, v167
	v_med3_f32 v170, v170, s16, v167
	v_med3_f32 v171, v171, s16, v167
	v_perm_b32 v168, v169, v168, s17
	v_perm_b32 v170, v171, v170, s26
	v_or_b32_e32 v150, v170, v168
	v_fma_f32 v168, v82, s15, v166
	v_fma_f32 v169, v86, s15, v166
	v_fma_f32 v170, v90, s15, v166
	v_fma_f32 v171, v94, s15, v166
	v_med3_f32 v168, v168, s16, v167
	v_med3_f32 v169, v169, s16, v167
	v_med3_f32 v170, v170, s16, v167
	v_med3_f32 v171, v171, s16, v167
	v_perm_b32 v168, v169, v168, s17
	v_perm_b32 v170, v171, v170, s26
	v_or_b32_e32 v151, v170, v168
	v_fma_f32 v168, v98, s15, v166
	v_fma_f32 v169, v102, s15, v166
	v_fma_f32 v170, v106, s15, v166
	v_fma_f32 v171, v110, s15, v166
	v_med3_f32 v168, v168, s16, v167
	v_med3_f32 v169, v169, s16, v167
	v_med3_f32 v170, v170, s16, v167
	v_med3_f32 v171, v171, s16, v167
	v_perm_b32 v168, v169, v168, s17
	v_perm_b32 v170, v171, v170, s26
	v_or_b32_e32 v152, v170, v168
	v_fma_f32 v168, v114, s15, v166
	v_fma_f32 v169, v118, s15, v166
	v_fma_f32 v170, v122, s15, v166
	v_fma_f32 v171, v126, s15, v166
	v_med3_f32 v168, v168, s16, v167
	v_med3_f32 v169, v169, s16, v167
	v_med3_f32 v170, v170, s16, v167
	v_med3_f32 v171, v171, s16, v167
	v_perm_b32 v168, v169, v168, s17
	v_perm_b32 v170, v171, v170, s26
	v_or_b32_e32 v153, v170, v168
	v_fma_f32 v168, v67, s15, v166
	v_fma_f32 v169, v71, s15, v166
	v_fma_f32 v170, v75, s15, v166
	v_fma_f32 v171, v79, s15, v166
	v_med3_f32 v168, v168, s16, v167
	v_med3_f32 v169, v169, s16, v167
	v_med3_f32 v170, v170, s16, v167
	v_med3_f32 v171, v171, s16, v167
	v_perm_b32 v168, v169, v168, s17
	v_perm_b32 v170, v171, v170, s26
	v_or_b32_e32 v154, v170, v168
	v_fma_f32 v168, v83, s15, v166
	v_fma_f32 v169, v87, s15, v166
	v_fma_f32 v170, v91, s15, v166
	v_fma_f32 v171, v95, s15, v166
	v_med3_f32 v168, v168, s16, v167
	v_med3_f32 v169, v169, s16, v167
	v_med3_f32 v170, v170, s16, v167
	v_med3_f32 v171, v171, s16, v167
	v_perm_b32 v168, v169, v168, s17
	v_perm_b32 v170, v171, v170, s26
	v_or_b32_e32 v155, v170, v168
	v_fma_f32 v168, v99, s15, v166
	v_fma_f32 v169, v103, s15, v166
	v_fma_f32 v170, v107, s15, v166
	v_fma_f32 v171, v111, s15, v166
	v_med3_f32 v168, v168, s16, v167
	v_med3_f32 v169, v169, s16, v167
	v_med3_f32 v170, v170, s16, v167
	v_med3_f32 v171, v171, s16, v167
	v_perm_b32 v168, v169, v168, s17
	v_perm_b32 v170, v171, v170, s26
	v_or_b32_e32 v156, v170, v168
	v_fma_f32 v168, v115, s15, v166
	v_fma_f32 v169, v119, s15, v166
	v_fma_f32 v170, v123, s15, v166
	v_fma_f32 v171, v127, s15, v166
	v_med3_f32 v168, v168, s16, v167
	v_med3_f32 v169, v169, s16, v167
	v_med3_f32 v170, v170, s16, v167
	v_med3_f32 v171, v171, s16, v167
	v_perm_b32 v168, v169, v168, s17
	v_perm_b32 v170, v171, v170, s26
	v_or_b32_e32 v157, v170, v168
	v_fma_f32 v168, v68, s15, v166
	v_fma_f32 v169, v72, s15, v166
	v_fma_f32 v170, v76, s15, v166
	v_fma_f32 v171, v80, s15, v166
	v_med3_f32 v168, v168, s16, v167
	v_med3_f32 v169, v169, s16, v167
	v_med3_f32 v170, v170, s16, v167
	v_med3_f32 v171, v171, s16, v167
	v_perm_b32 v168, v169, v168, s17
	v_perm_b32 v170, v171, v170, s26
	v_or_b32_e32 v158, v170, v168
	v_fma_f32 v168, v84, s15, v166
	v_fma_f32 v169, v88, s15, v166
	v_fma_f32 v170, v92, s15, v166
	v_fma_f32 v171, v96, s15, v166
	v_med3_f32 v168, v168, s16, v167
	v_med3_f32 v169, v169, s16, v167
	v_med3_f32 v170, v170, s16, v167
	v_med3_f32 v171, v171, s16, v167
	v_perm_b32 v168, v169, v168, s17
	v_perm_b32 v170, v171, v170, s26
	v_or_b32_e32 v159, v170, v168
	v_fma_f32 v168, v100, s15, v166
	v_fma_f32 v169, v104, s15, v166
	v_fma_f32 v170, v108, s15, v166
	v_fma_f32 v171, v112, s15, v166
	v_med3_f32 v168, v168, s16, v167
	v_med3_f32 v169, v169, s16, v167
	v_med3_f32 v170, v170, s16, v167
	v_med3_f32 v171, v171, s16, v167
	v_perm_b32 v168, v169, v168, s17
	v_perm_b32 v170, v171, v170, s26
	v_or_b32_e32 v160, v170, v168
	v_fma_f32 v168, v116, s15, v166
	v_fma_f32 v169, v120, s15, v166
	v_fma_f32 v170, v124, s15, v166
	v_fma_f32 v171, v128, s15, v166
	v_med3_f32 v168, v168, s16, v167
	v_med3_f32 v169, v169, s16, v167
	v_med3_f32 v170, v170, s16, v167
	v_med3_f32 v171, v171, s16, v167
	v_perm_b32 v168, v169, v168, s17
	v_perm_b32 v170, v171, v170, s26
	v_or_b32_e32 v161, v170, v168
	v_fma_f32 v168, v69, s15, v166
	v_fma_f32 v169, v73, s15, v166
	v_fma_f32 v170, v77, s15, v166
	v_fma_f32 v171, v81, s15, v166
	v_med3_f32 v168, v168, s16, v167
	v_med3_f32 v169, v169, s16, v167
	v_med3_f32 v170, v170, s16, v167
	v_med3_f32 v171, v171, s16, v167
	v_perm_b32 v168, v169, v168, s17
	v_perm_b32 v170, v171, v170, s26
	v_or_b32_e32 v162, v170, v168
	v_fma_f32 v168, v85, s15, v166
	v_fma_f32 v169, v89, s15, v166
	v_fma_f32 v170, v93, s15, v166
	v_fma_f32 v171, v97, s15, v166
	v_med3_f32 v168, v168, s16, v167
	v_med3_f32 v169, v169, s16, v167
	v_med3_f32 v170, v170, s16, v167
	v_med3_f32 v171, v171, s16, v167
	v_perm_b32 v168, v169, v168, s17
	v_perm_b32 v170, v171, v170, s26
	v_or_b32_e32 v163, v170, v168
	v_fma_f32 v168, v101, s15, v166
	v_fma_f32 v169, v105, s15, v166
	v_fma_f32 v170, v109, s15, v166
	v_fma_f32 v171, v113, s15, v166
	v_med3_f32 v168, v168, s16, v167
	v_med3_f32 v169, v169, s16, v167
	v_med3_f32 v170, v170, s16, v167
	v_med3_f32 v171, v171, s16, v167
	v_perm_b32 v168, v169, v168, s17
	v_perm_b32 v170, v171, v170, s26
	v_or_b32_e32 v164, v170, v168
	v_fma_f32 v168, v117, s15, v166
	v_fma_f32 v169, v121, s15, v166
	v_fma_f32 v170, v125, s15, v166
	v_fma_f32 v171, v129, s15, v166
	v_med3_f32 v168, v168, s16, v167
	v_med3_f32 v169, v169, s16, v167
	v_med3_f32 v170, v170, s16, v167
	v_med3_f32 v171, v171, s16, v167
	v_perm_b32 v168, v169, v168, s17
	v_perm_b32 v170, v171, v170, s26
	v_or_b32_e32 v165, v170, v168
	global_store_dwordx4 v146, v[150:153], s[10:11]
	global_store_dwordx4 v147, v[154:157], s[10:11]
	global_store_dwordx4 v148, v[158:161], s[10:11]
	global_store_dwordx4 v149, v[162:165], s[10:11]
	s_branch .Lq_done
.Lq_tailA:
	s_waitcnt vmcnt(0)
	v_fma_f32 v168, v2, s15, v166
	v_fma_f32 v169, v6, s15, v166
	v_fma_f32 v170, v10, s15, v166
	v_fma_f32 v171, v14, s15, v166
	v_med3_f32 v168, v168, s16, v167
	v_med3_f32 v169, v169, s16, v167
	v_med3_f32 v170, v170, s16, v167
	v_med3_f32 v171, v171, s16, v167
	v_perm_b32 v168, v169, v168, s17
	v_perm_b32 v170, v171, v170, s26
	v_or_b32_e32 v150, v170, v168
	v_fma_f32 v168, v18, s15, v166
	v_fma_f32 v169, v22, s15, v166
	v_fma_f32 v170, v26, s15, v166
	v_fma_f32 v171, v30, s15, v166
	v_med3_f32 v168, v168, s16, v167
	v_med3_f32 v169, v169, s16, v167
	v_med3_f32 v170, v170, s16, v167
	v_med3_f32 v171, v171, s16, v167
	v_perm_b32 v168, v169, v168, s17
	v_perm_b32 v170, v171, v170, s26
	v_or_b32_e32 v151, v170, v168
	v_fma_f32 v168, v34, s15, v166
	v_fma_f32 v169, v38, s15, v166
	v_fma_f32 v170, v42, s15, v166
	v_fma_f32 v171, v46, s15, v166
	v_med3_f32 v168, v168, s16, v167
	v_med3_f32 v169, v169, s16, v167
	v_med3_f32 v170, v170, s16, v167
	v_med3_f32 v171, v171, s16, v167
	v_perm_b32 v168, v169, v168, s17
	v_perm_b32 v170, v171, v170, s26
	v_or_b32_e32 v152, v170, v168
	v_fma_f32 v168, v50, s15, v166
	v_fma_f32 v169, v54, s15, v166
	v_fma_f32 v170, v58, s15, v166
	v_fma_f32 v171, v62, s15, v166
	v_med3_f32 v168, v168, s16, v167
	v_med3_f32 v169, v169, s16, v167
	v_med3_f32 v170, v170, s16, v167
	v_med3_f32 v171, v171, s16, v167
	v_perm_b32 v168, v169, v168, s17
	v_perm_b32 v170, v171, v170, s26
	v_or_b32_e32 v153, v170, v168
	v_fma_f32 v168, v3, s15, v166
	v_fma_f32 v169, v7, s15, v166
	v_fma_f32 v170, v11, s15, v166
	v_fma_f32 v171, v15, s15, v166
	v_med3_f32 v168, v168, s16, v167
	v_med3_f32 v169, v169, s16, v167
	v_med3_f32 v170, v170, s16, v167
	v_med3_f32 v171, v171, s16, v167
	v_perm_b32 v168, v169, v168, s17
	v_perm_b32 v170, v171, v170, s26
	v_or_b32_e32 v154, v170, v168
	v_fma_f32 v168, v19, s15, v166
	v_fma_f32 v169, v23, s15, v166
	v_fma_f32 v170, v27, s15, v166
	v_fma_f32 v171, v31, s15, v166
	v_med3_f32 v168, v168, s16, v167
	v_med3_f32 v169, v169, s16, v167
	v_med3_f32 v170, v170, s16, v167
	v_med3_f32 v171, v171, s16, v167
	v_perm_b32 v168, v169, v168, s17
	v_perm_b32 v170, v171, v170, s26
	v_or_b32_e32 v155, v170, v168
	v_fma_f32 v168, v35, s15, v166
	v_fma_f32 v169, v39, s15, v166
	v_fma_f32 v170, v43, s15, v166
	v_fma_f32 v171, v47, s15, v166
	v_med3_f32 v168, v168, s16, v167
	v_med3_f32 v169, v169, s16, v167
	v_med3_f32 v170, v170, s16, v167
	v_med3_f32 v171, v171, s16, v167
	v_perm_b32 v168, v169, v168, s17
	v_perm_b32 v170, v171, v170, s26
	v_or_b32_e32 v156, v170, v168
	v_fma_f32 v168, v51, s15, v166
	v_fma_f32 v169, v55, s15, v166
	v_fma_f32 v170, v59, s15, v166
	v_fma_f32 v171, v63, s15, v166
	v_med3_f32 v168, v168, s16, v167
	v_med3_f32 v169, v169, s16, v167
	v_med3_f32 v170, v170, s16, v167
	v_med3_f32 v171, v171, s16, v167
	v_perm_b32 v168, v169, v168, s17
	v_perm_b32 v170, v171, v170, s26
	v_or_b32_e32 v157, v170, v168
	v_fma_f32 v168, v4, s15, v166
	v_fma_f32 v169, v8, s15, v166
	v_fma_f32 v170, v12, s15, v166
	v_fma_f32 v171, v16, s15, v166
	v_med3_f32 v168, v168, s16, v167
	v_med3_f32 v169, v169, s16, v167
	v_med3_f32 v170, v170, s16, v167
	v_med3_f32 v171, v171, s16, v167
	v_perm_b32 v168, v169, v168, s17
	v_perm_b32 v170, v171, v170, s26
	v_or_b32_e32 v158, v170, v168
	v_fma_f32 v168, v20, s15, v166
	v_fma_f32 v169, v24, s15, v166
	v_fma_f32 v170, v28, s15, v166
	v_fma_f32 v171, v32, s15, v166
	v_med3_f32 v168, v168, s16, v167
	v_med3_f32 v169, v169, s16, v167
	v_med3_f32 v170, v170, s16, v167
	v_med3_f32 v171, v171, s16, v167
	v_perm_b32 v168, v169, v168, s17
	v_perm_b32 v170, v171, v170, s26
	v_or_b32_e32 v159, v170, v168
	v_fma_f32 v168, v36, s15, v166
	v_fma_f32 v169, v40, s15, v166
	v_fma_f32 v170, v44, s15, v166
	v_fma_f32 v171, v48, s15, v166
	v_med3_f32 v168, v168, s16, v167
	v_med3_f32 v169, v169, s16, v167
	v_med3_f32 v170, v170, s16, v167
	v_med3_f32 v171, v171, s16, v167
	v_perm_b32 v168, v169, v168, s17
	v_perm_b32 v170, v171, v170, s26
	v_or_b32_e32 v160, v170, v168
	v_fma_f32 v168, v52, s15, v166
	v_fma_f32 v169, v56, s15, v166
	v_fma_f32 v170, v60, s15, v166
	v_fma_f32 v171, v64, s15, v166
	v_med3_f32 v168, v168, s16, v167
	v_med3_f32 v169, v169, s16, v167
	v_med3_f32 v170, v170, s16, v167
	v_med3_f32 v171, v171, s16, v167
	v_perm_b32 v168, v169, v168, s17
	v_perm_b32 v170, v171, v170, s26
	v_or_b32_e32 v161, v170, v168
	v_fma_f32 v168, v5, s15, v166
	v_fma_f32 v169, v9, s15, v166
	v_fma_f32 v170, v13, s15, v166
	v_fma_f32 v171, v17, s15, v166
	v_med3_f32 v168, v168, s16, v167
	v_med3_f32 v169, v169, s16, v167
	v_med3_f32 v170, v170, s16, v167
	v_med3_f32 v171, v171, s16, v167
	v_perm_b32 v168, v169, v168, s17
	v_perm_b32 v170, v171, v170, s26
	v_or_b32_e32 v162, v170, v168
	v_fma_f32 v168, v21, s15, v166
	v_fma_f32 v169, v25, s15, v166
	v_fma_f32 v170, v29, s15, v166
	v_fma_f32 v171, v33, s15, v166
	v_med3_f32 v168, v168, s16, v167
	v_med3_f32 v169, v169, s16, v167
	v_med3_f32 v170, v170, s16, v167
	v_med3_f32 v171, v171, s16, v167
	v_perm_b32 v168, v169, v168, s17
	v_perm_b32 v170, v171, v170, s26
	v_or_b32_e32 v163, v170, v168
	v_fma_f32 v168, v37, s15, v166
	v_fma_f32 v169, v41, s15, v166
	v_fma_f32 v170, v45, s15, v166
	v_fma_f32 v171, v49, s15, v166
	v_med3_f32 v168, v168, s16, v167
	v_med3_f32 v169, v169, s16, v167
	v_med3_f32 v170, v170, s16, v167
	v_med3_f32 v171, v171, s16, v167
	v_perm_b32 v168, v169, v168, s17
	v_perm_b32 v170, v171, v170, s26
	v_or_b32_e32 v164, v170, v168
	v_fma_f32 v168, v53, s15, v166
	v_fma_f32 v169, v57, s15, v166
	v_fma_f32 v170, v61, s15, v166
	v_fma_f32 v171, v65, s15, v166
	v_med3_f32 v168, v168, s16, v167
	v_med3_f32 v169, v169, s16, v167
	v_med3_f32 v170, v170, s16, v167
	v_med3_f32 v171, v171, s16, v167
	v_perm_b32 v168, v169, v168, s17
	v_perm_b32 v170, v171, v170, s26
	v_or_b32_e32 v165, v170, v168
	global_store_dwordx4 v146, v[150:153], s[8:9]
	global_store_dwordx4 v147, v[154:157], s[8:9]
	global_store_dwordx4 v148, v[158:161], s[8:9]
	global_store_dwordx4 v149, v[162:165], s[8:9]
.Lq_done:
	s_waitcnt vmcnt(0)
	s_cmp_eq_u32 s46, 2
	s_cbranch_scc1 .LBB0_251
	s_cmp_eq_u32 s46, 7
	s_cbranch_scc1 .LBB0_771
	s_cmp_eq_u32 s46, 10
	s_cbranch_scc1 .LBB0_1212
	s_cmp_eq_u32 s46, 12
	s_cbranch_scc1 .Lq2_gemm
	s_cmp_eq_u32 s46, 17
	s_cbranch_scc1 .Lq7_gemm
	s_branch .Lq10_gemm
.Lq_skip:
.LBB0_754:
	v_readlane_b32 s2, v250, 40
	v_readlane_b32 s3, v250, 41
	s_cmp_lt_i32 s2, 8
	s_cselect_b64 s[2:3], -1, 0
	s_and_b64 s[0:1], s[2:3], s[0:1]
	s_andn2_b64 vcc, exec, s[0:1]
	s_cbranch_vccnz .LBB0_805
	s_cmp_eq_u32 s97, 0x100
	s_cselect_b32 s98, 202, s97
	v_readfirstlane_b32 s30, v0
	s_lshr_b32 s30, s30, 6
	s_cmp_eq_u32 s97, 0x100
	s_cbranch_scc0 .Lq7_all
	s_cmpk_lt_i32 s74, 202
	s_cbranch_scc1 .Lq7_gemm
	s_sub_u32 s12, s74, 202
	s_lshl_b32 s12, s12, 3
	s_add_u32 s12, s12, s30
	s_add_u32 s12, s12, 0x5328
	s_movk_i32 s13, 432
	s_mov_b32 s14, 0x97e8
	s_mov_b32 s46, 7
	s_branch .Lq_conv
.Lq7_all:
	s_lshl_b32 s12, s74, 3
	s_add_u32 s12, s12, s30
	s_add_u32 s12, s12, 0x5328
	s_lshl_b32 s13, s97, 3
	s_mov_b32 s14, 0x97e8
	s_mov_b32 s46, 17
	s_branch .Lq_conv
.Lq7_gemm:
	s_cmpk_gt_i32 s74, 0x57f
	v_readfirstlane_b32 s1, v0
	s_cbranch_scc1 .LBB0_771
	s_waitcnt vmcnt(16)
	v_lshrrev_b32_e32 v2, 5, v0
	v_lshrrev_b32_e32 v4, 1, v0
	v_and_b32_e32 v2, 4, v2
	v_bfe_u32 v3, v0, 2, 2
	s_waitcnt vmcnt(14)
	v_and_b32_e32 v13, 24, v4
	v_or3_b32 v2, v2, v3, v13
	v_lshlrev_b32_e32 v3, 4, v0
	v_or_b32_e32 v10, 0x2000, v3
	s_add_u32 s30, s78, 0x1b00000
	v_lshrrev_b32_e32 v4, 7, v10
	s_movk_i32 s0, 0x60
	s_addc_u32 s31, s79, 0
	v_and_or_b32 v5, v4, s0, v2
	s_waitcnt vmcnt(13)
	v_bfe_u32 v14, v0, 2, 4
	s_movk_i32 s0, 0x70
	s_ashr_i32 s34, s74, 31
	v_and_or_b32 v4, v4, s0, v14
	s_lshr_b32 s0, s34, 29
	s_add_i32 s0, s74, s0
	s_lshr_b32 s10, s1, 6
	s_and_b32 s4, s0, -8
	s_lshr_b32 s12, s1, 8
	s_lshl_b32 s33, s10, 10
	s_sub_i32 s4, s74, s4
	s_cmp_lt_i32 s4, 0
	s_movk_i32 s35, 0xb1
	s_cselect_b32 s5, s35, 0xb0
	s_mul_i32 s4, s4, s5
	s_ashr_i32 s0, s0, 3
	s_add_i32 s4, s4, s0
	s_mul_hi_i32 s0, s4, 0x2e8ba2e9
	s_lshr_b32 s5, s0, 31
	s_ashr_i32 s0, s0, 6
	s_add_i32 s0, s0, s5
	s_lshl_b32 s5, s0, 3
	s_mulk_i32 s0, 0x160
	s_sub_i32 s4, s4, s0
	s_sext_i32_i16 s0, s4
	s_bfe_u32 s0, s0, 0x3001c
	s_add_i32 s6, s4, s0
	s_sext_i32_i16 s0, s6
	s_and_b32 s6, s6, 0xfff8
	s_sub_i32 s4, s4, s6
	s_sext_i32_i16 s4, s4
	v_and_b32_e32 v6, 32, v0
	s_lshr_b32 s0, s0, 3
	s_add_i32 s22, s5, s4
	v_bitop3_b32 v11, v3, v6, 48 bitop3:0x6c
	v_and_b32_e32 v12, 64, v0
	s_ashr_i32 s23, s22, 31
	s_bfe_i64 s[6:7], s[0:1], 0x100000
	v_or_b32_e32 v3, v11, v12
	s_lshl_b64 s[4:5], s[22:23], 19
	s_lshl_b64 s[6:7], s[6:7], 19
	v_lshl_or_b32 v164, v4, 11, v3
	v_lshrrev_b32_e32 v4, 3, v0
	s_add_u32 s26, s30, s6
	v_and_or_b32 v2, v4, 32, v2
	s_addc_u32 s27, s31, s7
	s_add_i32 s23, s33, 0
	v_lshl_or_b32 v166, v2, 11, v3
	s_add_i32 m0, s23, 0x10000
	v_lshl_or_b32 v162, v5, 11, v3
	global_load_lds_dwordx4 v166, s[26:27]
	s_add_i32 m0, s23, 0x12000
	s_add_u32 s6, s26, 0x40000
	global_load_lds_dwordx4 v162, s[26:27]
	s_addc_u32 s7, s27, 0
	s_add_i32 m0, s23, 0x14000
	v_and_or_b32 v2, v4, 48, v14
	global_load_lds_dwordx4 v166, s[6:7]
	s_add_i32 m0, s23, 0x16000
	s_add_u32 s24, s72, s4
	s_addc_u32 s25, s73, s5
	s_add_i32 s36, s23, 0x2000
	v_lshl_or_b32 v168, v2, 11, v3
	global_load_lds_dwordx4 v162, s[6:7]
	s_mov_b32 m0, s23
	s_add_u32 s4, s24, 0x40000
	global_load_lds_dwordx4 v168, s[24:25]
	s_mov_b32 m0, s36
	s_addc_u32 s5, s25, 0
	s_add_i32 s37, s23, 0x4000
	v_mov_b32_e32 v1, 0x5cba0000
	global_load_lds_dwordx4 v164, s[24:25]
	s_mov_b32 m0, s37
	s_add_i32 s38, s23, 0x6000
	global_load_dword v1, v1, s[78:79] offset:8
	v_mov_b32_e32 v167, 0
	global_load_lds_dwordx4 v168, s[4:5]
	s_mov_b32 m0, s38
	v_mov_b32_e32 v163, v167
	global_load_lds_dwordx4 v164, s[4:5]
	v_mov_b32_e32 v169, v167
	v_mov_b32_e32 v165, v167
	s_cmp_eq_u32 s12, 1
	s_mov_b32 s39, 0
	v_lshl_add_u64 v[8:9], s[26:27], 0, v[166:167]
	v_lshl_add_u64 v[6:7], s[26:27], 0, v[162:163]
	v_lshl_add_u64 v[2:3], s[24:25], 0, v[168:169]
	s_cselect_b64 s[4:5], -1, 0
	s_cmp_lg_u32 s12, 1
	v_lshl_add_u64 v[4:5], s[24:25], 0, v[164:165]
	s_cbranch_scc1 .LBB0_758
	s_barrier

.LBB0_761:
	s_add_i32 s39, s39, 1
	s_mul_i32 s0, s39, s42
	s_mul_hi_u32 s1, s39, s98
	s_add_i32 s1, s1, s0
	s_mul_i32 s0, s39, s98
	s_add_u32 s18, s0, s74
	s_addc_u32 s19, s1, s34
	v_cmp_gt_i64_e32 vcc, s[18:19], v[176:177]
	v_cmp_lt_i64_e64 s[0:1], s[18:19], v[174:175]
	s_cbranch_vccnz .LBB0_763
	s_ashr_i32 s14, s18, 31
	s_lshr_b32 s14, s14, 29
	s_add_i32 s14, s18, s14
	s_ashr_i32 s15, s14, 3
	s_and_b32 s14, s14, -8
	s_sub_i32 s14, s18, s14
	s_cmp_lt_i32 s14, 0
	s_cselect_b32 s16, s35, 0xb0
	s_mul_i32 s14, s14, s16
	s_add_i32 s14, s14, s15
	s_mul_hi_i32 s15, s14, 0x2e8ba2e9
	s_lshr_b32 s16, s15, 31
	s_ashr_i32 s15, s15, 6
	s_add_i32 s15, s15, s16
	s_lshl_b32 s16, s15, 3
	s_sub_i32 s17, 32, s16
	s_min_i32 s17, s17, 8
	s_abs_i32 s18, s17
	v_cvt_f32_u32_e32 v2, s18
	s_sub_i32 s20, 0, s18
	s_mulk_i32 s15, 0x160
	s_sub_i32 s15, s14, s15
	v_rcp_iflag_f32_e32 v2, v2
	s_abs_i32 s14, s15
	s_xor_b32 s19, s15, s17
	s_ashr_i32 s19, s19, 31
	v_mul_f32_e32 v2, 0x4f7ffffe, v2
	v_cvt_u32_f32_e32 v2, v2
	s_nop 0
	v_readfirstlane_b32 s21, v2
	s_mul_i32 s20, s20, s21
	s_mul_hi_u32 s20, s21, s20
	s_add_i32 s21, s21, s20
	s_mul_hi_u32 s20, s14, s21
	s_mul_i32 s21, s20, s18
	s_sub_i32 s14, s14, s21
	s_add_i32 s28, s20, 1
	s_sub_i32 s21, s14, s18
	s_cmp_ge_u32 s14, s18
	s_cselect_b32 s20, s28, s20
	s_cselect_b32 s14, s21, s14
	s_add_i32 s21, s20, 1
	s_cmp_ge_u32 s14, s18
	s_cselect_b32 s14, s21, s20
	s_xor_b32 s14, s14, s19
	s_sub_i32 s14, s14, s19
	s_mul_i32 s17, s14, s17
	s_sub_i32 s15, s15, s17
	s_add_i32 s16, s16, s15

.LBB0_771:
	v_readlane_b32 s0, v250, 44
	v_readlane_b32 s1, v250, 45
	s_andn2_b64 vcc, exec, s[0:1]
	s_cbranch_vccnz .LBB0_805
	s_abs_i32 s0, s97
	v_cvt_f32_u32_e32 v1, s0
	s_sub_i32 s5, 0, s0
	s_add_i32 s1, s97, 0x57f
	s_xor_b32 s4, s1, s97
	v_rcp_iflag_f32_e32 v1, v1
	s_abs_i32 s1, s1
	s_ashr_i32 s4, s4, 31
	v_mul_f32_e32 v1, 0x4f7ffffe, v1
	v_cvt_u32_f32_e32 v1, v1
	s_nop 0
	v_readfirstlane_b32 s6, v1
	s_mul_i32 s5, s5, s6
	s_mul_hi_u32 s5, s6, s5
	s_add_i32 s6, s6, s5
	s_mul_hi_u32 s5, s1, s6
	s_mul_i32 s6, s5, s0
	s_sub_i32 s1, s1, s6
	s_add_i32 s7, s5, 1
	s_sub_i32 s6, s1, s0
	s_cmp_ge_u32 s1, s0
	s_cselect_b32 s5, s7, s5
	s_cselect_b32 s1, s6, s1
	s_add_i32 s6, s5, 1
	s_cmp_ge_u32 s1, s0
	s_cselect_b32 s0, s6, s5
	s_not_b32 s1, s4
	s_xor_b32 s0, s0, s4
	s_add_i32 s0, s1, s0
	s_mul_i32 s0, s0, s97
	s_sub_i32 s4, 0x580, s0
	s_cmp_ge_i32 s4, s97
	s_cselect_b64 s[0:1], -1, 0
	s_cmp_lt_i32 s74, s4
	s_cselect_b64 s[4:5], -1, 0
	s_or_b64 s[0:1], s[0:1], s[4:5]
	s_and_b64 vcc, exec, s[0:1]
	s_cbranch_vccnz .LBB0_805
	s_cmp_gt_i32 s75, 0x2fff
	s_cbranch_scc1 .LBB0_805
	v_readlane_b32 s0, v250, 55
	s_waitcnt vmcnt(16)
	v_and_b32_e32 v2, 7, v0
	v_lshrrev_b32_e32 v3, 3, v178
	s_xor_b32 s14, s0, 0x80000000
	s_cmp_gt_i32 s75, 0xdfff
	v_lshlrev_b32_e32 v1, 4, v3
	v_lshlrev_b32_e32 v134, 2, v2
	v_lshlrev_b32_e32 v2, 4, v2
	s_cbranch_scc0 .LBB0_776
	s_add_i32 s0, s75, 0x2000
	s_bfe_u32 s1, s0, 0x70009
	s_mulk_i32 s1, 0x2493
	s_lshr_b32 s7, s1, 16
	s_mul_i32 s1, s7, 0xe00
	s_sub_i32 s0, s0, s1
	v_readlane_b32 s16, v250, 32
	s_and_b32 s0, s0, 0xffff
	s_mul_i32 s4, s7, 0x3800000
	v_readlane_b32 s22, v250, 38
	v_readlane_b32 s23, v250, 39
	s_add_u32 s4, s22, s4
	s_addc_u32 s5, s23, 0
	s_lshl_b32 s6, s0, 1
	s_and_b32 s6, s6, 0x1f80
	v_lshlrev_b32_e32 v136, 4, v3
	v_or_b32_e32 v3, s6, v136
	v_lshlrev_b32_e32 v4, 13, v3
	v_mov_b32_e32 v5, 0
	s_lshl_b32 s0, s0, 5
	s_waitcnt vmcnt(15)
	v_lshl_add_u64 v[6:7], s[4:5], 0, v[4:5]
	s_and_b32 s4, s0, 0x7e0
	s_mov_b32 s1, 0
	s_lshl_b32 s0, s4, 2
	v_lshl_add_u64 v[6:7], v[6:7], 0, s[0:1]
	s_lshl_b32 s0, s7, 11
	v_mov_b32_e32 v3, v5
	s_or_b32 s0, s0, s4
	v_mov_b32_e32 v135, v5
	v_lshl_add_u64 v[6:7], v[6:7], 0, v[2:3]
	v_or_b32_e32 v3, s0, v134
	s_movk_i32 s0, 0x1c00
	v_mov_b64_e32 v[4:5], s[78:79]
	v_mad_u64_u32 v[4:5], s[4:5], v3, s0, v[4:5]
	s_mov_b32 s7, s1
	v_lshl_add_u64 v[4:5], v[4:5], 0, s[6:7]
	s_mov_b64 s[0:1], 0x24500000
	v_readlane_b32 s17, v250, 33
	v_readlane_b32 s18, v250, 34
	v_readlane_b32 s19, v250, 35
	v_readlane_b32 s20, v250, 36
	v_readlane_b32 s21, v250, 37
	v_lshl_add_u64 v[66:67], v[4:5], 0, s[0:1]
	s_mov_b64 s[0:1], 0
	s_mov_b32 s15, 0x43000000
	s_branch .LBB0_777

.LBB0_782:
	s_cmp_gt_i32 s17, 0
	s_cselect_b64 s[0:1], -1, 0
	s_cmp_lt_i32 s75, 0x3000
	s_cselect_b64 s[12:13], -1, 0
	s_and_b64 s[12:13], s[0:1], s[12:13]
	v_cndmask_b32_e64 v130, 0, 1, s[12:13]
	v_cmp_ne_u32_e64 s[0:1], 1, v130
	s_andn2_b64 vcc, exec, s[12:13]
	s_cbranch_vccnz .LBB0_789
	s_cmp_gt_i32 s75, 0xdfff
	s_mov_b64 s[10:11], -1
	s_cbranch_scc0 .LBB0_785
	s_add_i32 s10, s75, 0x2000
	s_bfe_u32 s11, s10, 0x70009
	s_mulk_i32 s11, 0x2493
	s_lshr_b32 s13, s11, 16
	s_mul_i32 s11, s13, 0xe00
	s_sub_i32 s10, s10, s11
	v_readlane_b32 s24, v250, 32
	s_and_b32 s21, s10, 0xffff
	s_mul_i32 s10, s13, 0x3800000
	v_readlane_b32 s30, v250, 38
	v_readlane_b32 s31, v250, 39
	s_add_u32 s10, s30, s10
	s_addc_u32 s11, s31, 0
	s_lshl_b32 s12, s21, 1
	s_and_b32 s12, s12, 0x1f80
	s_waitcnt vmcnt(16)
	v_or_b32_e32 v66, s12, v136
	v_lshlrev_b32_e32 v138, 13, v66
	v_lshl_add_u64 v[66:67], s[10:11], 0, v[138:139]
	s_lshl_b32 s10, s21, 5
	s_and_b32 s21, s10, 0x7e0
	s_lshl_b32 s10, s21, 2
	s_mov_b32 s11, s5
	v_lshl_add_u64 v[66:67], v[66:67], 0, s[10:11]
	s_lshl_b32 s10, s13, 11
	s_or_b32 s10, s10, s21
	v_or_b32_e32 v68, s10, v134
	v_mul_hi_i32_i24_e32 v69, 0x1c00, v68
	v_mul_i32_i24_e32 v68, 0x1c00, v68
	v_lshl_add_u64 v[68:69], s[6:7], 0, v[68:69]
	s_mov_b32 s13, s5
	v_readlane_b32 s25, v250, 33
	v_readlane_b32 s26, v250, 34
	v_readlane_b32 s27, v250, 35
	v_readlane_b32 s28, v250, 36
	v_readlane_b32 s29, v250, 37
	v_lshl_add_u64 v[130:131], v[68:69], 0, s[12:13]
	s_mov_b64 s[10:11], 0

.LBB0_793:
	v_mad_u64_u32 v[144:145], s[12:13], s4, 3, v[140:141]
	s_and_b64 vcc, exec, s[0:1]
	s_mov_b64 s[0:1], 0
	global_store_dwordx4 v[144:145], v[130:133], off
	s_cbranch_vccnz .LBB0_781
	s_cmp_gt_i32 s17, 0
	s_cselect_b64 s[0:1], -1, 0
	s_cmp_lt_i32 s75, 0x3000
	s_cselect_b64 s[12:13], -1, 0
	s_and_b64 s[0:1], s[0:1], s[12:13]
	s_andn2_b64 vcc, exec, s[0:1]
	s_cbranch_vccnz .LBB0_801
	s_cmp_gt_i32 s75, 0xdfff
	s_mov_b64 s[12:13], -1
	s_cbranch_scc0 .LBB0_797
	s_add_i32 s4, s75, 0x2000
	s_bfe_u32 s11, s4, 0x70009
	s_mulk_i32 s11, 0x2493
	s_lshr_b32 s11, s11, 16
	s_mul_i32 s12, s11, 0xe00
	s_sub_i32 s4, s4, s12
	v_readlane_b32 s24, v250, 32
	s_and_b32 s4, s4, 0xffff
	s_mul_i32 s12, s11, 0x3800000
	v_readlane_b32 s30, v250, 38
	v_readlane_b32 s31, v250, 39
	s_add_u32 s12, s30, s12
	s_addc_u32 s13, s31, 0
	s_lshl_b32 s15, s4, 1
	s_and_b32 s22, s15, 0x1f80
	s_waitcnt vmcnt(16)
	v_or_b32_e32 v2, s22, v136
	v_lshlrev_b32_e32 v138, 13, v2
	s_lshl_b32 s4, s4, 5
	v_lshl_add_u64 v[2:3], s[12:13], 0, v[138:139]
	s_and_b32 s12, s4, 0x7e0
	s_lshl_b32 s4, s12, 2
	v_lshl_add_u64 v[2:3], v[2:3], 0, s[4:5]
	s_lshl_b32 s4, s11, 11
	s_or_b32 s4, s4, s12
	v_or_b32_e32 v4, s4, v134
	v_mul_hi_i32_i24_e32 v5, 0x1c00, v4
	v_mul_i32_i24_e32 v4, 0x1c00, v4
	v_lshl_add_u64 v[4:5], s[6:7], 0, v[4:5]
	s_mov_b32 s23, s5
	v_readlane_b32 s25, v250, 33
	v_readlane_b32 s26, v250, 34
	v_readlane_b32 s27, v250, 35
	v_readlane_b32 s28, v250, 36
	v_readlane_b32 s29, v250, 37
	v_lshl_add_u64 v[130:131], v[4:5], 0, s[22:23]
	s_mov_b64 s[12:13], 0

.LBB0_1185:
	v_readlane_b32 s0, v250, 40
	v_readlane_b32 s1, v250, 41
	s_cmp_lt_i32 s0, 11
	s_cselect_b64 s[2:3], -1, 0
	s_cmp_gt_i32 s1, 10
	s_cselect_b64 s[0:1], -1, 0
	s_and_b64 s[4:5], s[2:3], s[0:1]
	s_andn2_b64 vcc, exec, s[4:5]
	s_cbranch_vccnz .LBB0_1246
	s_cmp_eq_u32 s97, 0x100
	s_cselect_b32 s98, 192, s97
	v_readfirstlane_b32 s30, v0
	s_lshr_b32 s30, s30, 6
	s_cmp_eq_u32 s97, 0x100
	s_cbranch_scc0 .Lq10_all
	s_cmpk_lt_i32 s74, 192
	s_cbranch_scc1 .Lq10_gemm
	s_sub_u32 s12, s74, 192
	s_lshl_b32 s12, s12, 3
	s_add_u32 s12, s12, s30
	s_add_u32 s12, s12, 0x97e8
	s_movk_i32 s13, 512
	s_mov_b32 s14, 0xe000
	s_mov_b32 s46, 10
	s_branch .Lq_conv
.Lq10_all:
	s_lshl_b32 s12, s74, 3
	s_add_u32 s12, s12, s30
	s_add_u32 s12, s12, 0x97e8
	s_lshl_b32 s13, s97, 3
	s_mov_b32 s14, 0xe000
	s_mov_b32 s46, 20
	s_branch .Lq_conv
.Lq10_gemm:
	s_cmpk_gt_i32 s74, 0x47f
	v_readfirstlane_b32 s10, v0
	s_cbranch_scc1 .LBB0_1212
	s_cmpk_gt_i32 s74, 0x2ff
	s_cbranch_scc0 .LBB0_1189
	s_and_b32 s0, s74, 7
	s_add_i32 s1, s74, 0xfd00
	s_mul_i32 s0, s0, 48
	s_bfe_u32 s1, s1, 0xd0003
	s_add_i32 s0, s1, s0
	s_mul_i32 s1, s0, 0x2aab
	s_lshr_b32 s1, s1, 20
	s_lshl_b32 s6, s1, 3
	s_and_b32 s6, s6, 0xfff8
	s_sub_i32 s7, 32, s6
	s_min_u32 s7, s7, 8
	v_cvt_f32_ubyte0_e32 v1, s7
	s_waitcnt vmcnt(16)
	v_rcp_iflag_f32_e32 v2, v1
	s_mulk_i32 s1, 0x60
	s_sub_i32 s8, s0, s1
	v_cvt_f32_ubyte0_e32 v3, s8
	v_mul_f32_e32 v2, v3, v2
	v_trunc_f32_e32 v2, v2
	v_cvt_u32_f32_e32 v4, v2
	v_fma_f32 v2, -v2, v1, v3
	v_cmp_ge_f32_e64 s[0:1], |v2|, v1
	s_cmp_lg_u64 s[0:1], 0
	v_readfirstlane_b32 s9, v4
	s_addc_u32 s11, s9, 0
	s_mul_i32 s11, s11, s7
	s_sub_i32 s7, s8, s11
	s_and_b32 s7, s7, 0xff
	s_add_i32 s6, s6, s7
	s_add_i32 s12, s6, 32
	s_cmp_lg_u64 s[0:1], 0
	s_addc_u32 s0, s9, 24
	s_and_b32 s16, s0, 0xff
	s_cbranch_execz .LBB0_1190
	s_branch .LBB0_1191

.LBB0_1196:
	s_add_i32 s38, s38, 1
	s_mul_i32 s0, s38, s41
	s_mul_hi_u32 s1, s38, s98
	s_add_i32 s1, s1, s0
	s_mul_i32 s0, s38, s98
	s_add_u32 s22, s0, s74
	s_addc_u32 s23, s1, s42
	v_cmp_gt_i64_e32 vcc, s[22:23], v[176:177]
	v_cmp_lt_i64_e64 s[0:1], s[22:23], v[174:175]
	s_cbranch_vccnz .LBB0_1201
	v_cmp_gt_i64_e32 vcc, s[22:23], v[184:185]
	s_mov_b64 s[24:25], -1
	s_cbranch_vccz .LBB0_1199
	s_add_i32 s14, s22, 0xfffffd00
	s_ashr_i32 s15, s14, 31
	s_lshr_b32 s15, s15, 29
	s_add_i32 s15, s14, s15
	s_ashr_i32 s18, s15, 3
	s_and_b32 s15, s15, -8
	s_sub_i32 s14, s14, s15
	s_cmp_lt_i32 s14, 0
	s_cselect_b32 s15, 49, 48
	s_mul_i32 s14, s14, s15
	s_add_i32 s14, s14, s18
	s_mul_hi_i32 s15, s14, 0x2aaaaaab
	s_lshr_b32 s18, s15, 31
	s_ashr_i32 s15, s15, 4
	s_add_i32 s15, s15, s18
	s_lshl_b32 s18, s15, 3
	s_sub_i32 s19, 32, s18
	s_min_i32 s19, s19, 8
	s_abs_i32 s23, s19
	v_cvt_f32_u32_e32 v2, s23
	s_sub_i32 s25, 0, s23
	s_mulk_i32 s15, 0x60
	s_sub_i32 s14, s14, s15
	v_rcp_iflag_f32_e32 v2, v2
	s_abs_i32 s15, s14
	s_xor_b32 s24, s14, s19
	s_ashr_i32 s24, s24, 31
	v_mul_f32_e32 v2, 0x4f7ffffe, v2
	v_cvt_u32_f32_e32 v2, v2
	s_nop 0
	v_readfirstlane_b32 s30, v2
	s_mul_i32 s25, s25, s30
	s_mul_hi_u32 s25, s30, s25
	s_add_i32 s30, s30, s25
	s_mul_hi_u32 s25, s15, s30
	s_mul_i32 s30, s25, s23
	s_sub_i32 s15, s15, s30
	s_add_i32 s31, s25, 1
	s_sub_i32 s30, s15, s23
	s_cmp_ge_u32 s15, s23
	s_cselect_b32 s25, s31, s25
	s_cselect_b32 s15, s30, s15
	s_add_i32 s30, s25, 1
	s_cmp_ge_u32 s15, s23
	s_cselect_b32 s15, s30, s25
	s_xor_b32 s15, s15, s24
	s_sub_i32 s15, s15, s24
	s_mul_i32 s19, s15, s19
	s_sub_i32 s14, s14, s19
	s_add_i32 s14, s14, s18
	s_add_i32 s18, s14, 32
	s_add_i32 s14, s15, 24
	s_mov_b64 s[24:25], 0

.LBB0_1212:
	v_readlane_b32 s0, v250, 44
	v_readlane_b32 s1, v250, 45
	s_andn2_b64 vcc, exec, s[0:1]
	s_cbranch_vccnz .LBB0_1246
	s_abs_i32 s0, s97
	v_cvt_f32_u32_e32 v1, s0
	s_sub_i32 s7, 0, s0
	s_add_i32 s1, s97, 0x47f
	s_xor_b32 s6, s1, s97
	v_rcp_iflag_f32_e32 v1, v1
	s_abs_i32 s1, s1
	s_ashr_i32 s6, s6, 31
	v_mul_f32_e32 v1, 0x4f7ffffe, v1
	v_cvt_u32_f32_e32 v1, v1
	s_nop 0
	v_readfirstlane_b32 s8, v1
	s_mul_i32 s7, s7, s8
	s_mul_hi_u32 s7, s8, s7
	s_add_i32 s8, s8, s7
	s_mul_hi_u32 s7, s1, s8
	s_mul_i32 s8, s7, s0
	s_sub_i32 s1, s1, s8
	s_add_i32 s9, s7, 1
	s_sub_i32 s8, s1, s0
	s_cmp_ge_u32 s1, s0
	s_cselect_b32 s7, s9, s7
	s_cselect_b32 s1, s8, s1
	s_add_i32 s8, s7, 1
	s_cmp_ge_u32 s1, s0
	s_cselect_b32 s0, s8, s7
	s_not_b32 s1, s6
	s_xor_b32 s0, s0, s6
	s_add_i32 s0, s1, s0
	s_mul_i32 s0, s0, s97
	s_sub_i32 s6, 0x480, s0
	s_cmp_ge_i32 s6, s97
	s_cselect_b64 s[0:1], -1, 0
	s_cmp_lt_i32 s74, s6
	s_cselect_b64 s[6:7], -1, 0
	s_or_b64 s[0:1], s[0:1], s[6:7]
	s_and_b64 vcc, exec, s[0:1]
	s_cbranch_vccnz .LBB0_1246
	s_cmp_gt_i32 s75, 0x2fff
	s_cbranch_scc1 .LBB0_1246
	v_readlane_b32 s0, v250, 55
	s_waitcnt vmcnt(0)
	v_and_b32_e32 v2, 7, v0
	v_lshrrev_b32_e32 v3, 3, v178
	s_xor_b32 s16, s0, 0x80000000
	s_cmp_gt_i32 s75, 0xdfff
	v_lshlrev_b32_e32 v1, 4, v3
	v_lshlrev_b32_e32 v134, 2, v2
	v_lshlrev_b32_e32 v2, 4, v2
	s_cbranch_scc0 .LBB0_1217
	s_add_i32 s0, s75, 0x2000
	s_bfe_u32 s1, s0, 0x70009
	s_mulk_i32 s1, 0x2493
	s_lshr_b32 s9, s1, 16
	s_mul_i32 s1, s9, 0xe00
	s_sub_i32 s0, s0, s1
	v_readlane_b32 s24, v250, 32
	s_and_b32 s0, s0, 0xffff
	s_mul_i32 s6, s9, 0x3800000
	v_readlane_b32 s30, v250, 38
	v_readlane_b32 s31, v250, 39
	s_add_u32 s6, s30, s6
	s_addc_u32 s7, s31, 0
	s_lshl_b32 s8, s0, 1
	s_and_b32 s8, s8, 0x1f80
	v_lshlrev_b32_e32 v136, 4, v3
	v_or_b32_e32 v3, s8, v136
	v_lshlrev_b32_e32 v4, 13, v3
	v_mov_b32_e32 v5, 0
	s_lshl_b32 s0, s0, 5
	v_lshl_add_u64 v[6:7], s[6:7], 0, v[4:5]
	s_and_b32 s6, s0, 0x7e0
	s_mov_b32 s1, 0
	s_lshl_b32 s0, s6, 2
	v_lshl_add_u64 v[6:7], v[6:7], 0, s[0:1]
	s_lshl_b32 s0, s9, 11
	v_mov_b32_e32 v3, v5
	s_or_b32 s0, s0, s6
	v_mov_b32_e32 v135, v5
	v_lshl_add_u64 v[6:7], v[6:7], 0, v[2:3]
	v_or_b32_e32 v3, s0, v134
	s_movk_i32 s0, 0x1c00
	v_mov_b64_e32 v[4:5], s[78:79]
	v_mad_u64_u32 v[4:5], s[6:7], v3, s0, v[4:5]
	s_mov_b32 s9, s1
	v_lshl_add_u64 v[4:5], v[4:5], 0, s[8:9]
	s_mov_b64 s[0:1], 0x24500000
	v_readlane_b32 s25, v250, 33
	v_readlane_b32 s26, v250, 34
	v_readlane_b32 s27, v250, 35
	v_readlane_b32 s28, v250, 36
	v_readlane_b32 s29, v250, 37
	v_lshl_add_u64 v[66:67], v[4:5], 0, s[0:1]
	s_mov_b64 s[0:1], 0
	s_mov_b32 s17, 0x43000000
	s_branch .LBB0_1218

.LBB0_1223:
	s_cmp_gt_i32 s19, 0
	s_cselect_b64 s[0:1], -1, 0
	s_cmp_lt_i32 s75, 0x3000
	s_cselect_b64 s[14:15], -1, 0
	s_and_b64 s[14:15], s[0:1], s[14:15]
	v_cndmask_b32_e64 v130, 0, 1, s[14:15]
	v_cmp_ne_u32_e64 s[0:1], 1, v130
	s_andn2_b64 vcc, exec, s[14:15]
	s_cbranch_vccnz .LBB0_1230
	s_cmp_gt_i32 s75, 0xdfff
	s_mov_b64 s[12:13], -1
	s_cbranch_scc0 .LBB0_1226
	s_add_i32 s12, s75, 0x2000
	s_bfe_u32 s13, s12, 0x70009
	s_mulk_i32 s13, 0x2493
	s_lshr_b32 s15, s13, 16
	s_mul_i32 s13, s15, 0xe00
	s_sub_i32 s12, s12, s13
	v_readlane_b32 s36, v250, 32
	s_and_b32 s25, s12, 0xffff
	s_mul_i32 s12, s15, 0x3800000
	v_readlane_b32 s42, v250, 38
	v_readlane_b32 s43, v250, 39
	s_add_u32 s12, s42, s12
	s_addc_u32 s13, s43, 0
	s_lshl_b32 s14, s25, 1
	s_and_b32 s14, s14, 0x1f80
	s_waitcnt vmcnt(16)
	v_or_b32_e32 v66, s14, v136
	v_lshlrev_b32_e32 v138, 13, v66
	v_lshl_add_u64 v[66:67], s[12:13], 0, v[138:139]
	s_lshl_b32 s12, s25, 5
	s_and_b32 s25, s12, 0x7e0
	s_lshl_b32 s12, s25, 2
	s_mov_b32 s13, s7
	v_lshl_add_u64 v[66:67], v[66:67], 0, s[12:13]
	s_lshl_b32 s12, s15, 11
	s_or_b32 s12, s12, s25
	v_or_b32_e32 v68, s12, v134
	v_mul_hi_i32_i24_e32 v69, 0x1c00, v68
	v_mul_i32_i24_e32 v68, 0x1c00, v68
	v_lshl_add_u64 v[68:69], s[8:9], 0, v[68:69]
	s_mov_b32 s15, s7
	v_readlane_b32 s37, v250, 33
	v_readlane_b32 s38, v250, 34
	v_readlane_b32 s39, v250, 35
	v_readlane_b32 s40, v250, 36
	v_readlane_b32 s41, v250, 37
	v_lshl_add_u64 v[130:131], v[68:69], 0, s[14:15]
	s_mov_b64 s[12:13], 0

.LBB0_1234:
	v_mad_u64_u32 v[144:145], s[14:15], s6, 3, v[140:141]
	s_and_b64 vcc, exec, s[0:1]
	s_mov_b64 s[0:1], 0
	global_store_dwordx4 v[144:145], v[130:133], off
	s_cbranch_vccnz .LBB0_1222
	s_cmp_gt_i32 s19, 0
	s_cselect_b64 s[0:1], -1, 0
	s_cmp_lt_i32 s75, 0x3000
	s_cselect_b64 s[14:15], -1, 0
	s_and_b64 s[0:1], s[0:1], s[14:15]
	s_andn2_b64 vcc, exec, s[0:1]
	s_cbranch_vccnz .LBB0_1242
	s_cmp_gt_i32 s75, 0xdfff
	s_mov_b64 s[14:15], -1
	s_cbranch_scc0 .LBB0_1238
	s_add_i32 s6, s75, 0x2000
	s_bfe_u32 s13, s6, 0x70009
	s_mulk_i32 s13, 0x2493
	s_lshr_b32 s13, s13, 16
	s_mul_i32 s14, s13, 0xe00
	s_sub_i32 s6, s6, s14
	v_readlane_b32 s36, v250, 32
	s_and_b32 s6, s6, 0xffff
	s_mul_i32 s14, s13, 0x3800000
	v_readlane_b32 s42, v250, 38
	v_readlane_b32 s43, v250, 39
	s_add_u32 s14, s42, s14
	s_addc_u32 s15, s43, 0
	s_lshl_b32 s17, s6, 1
	s_and_b32 s26, s17, 0x1f80
	s_waitcnt vmcnt(16)
	v_or_b32_e32 v2, s26, v136
	v_lshlrev_b32_e32 v138, 13, v2
	s_lshl_b32 s6, s6, 5
	v_lshl_add_u64 v[2:3], s[14:15], 0, v[138:139]
	s_and_b32 s14, s6, 0x7e0
	s_lshl_b32 s6, s14, 2
	v_lshl_add_u64 v[2:3], v[2:3], 0, s[6:7]
	s_lshl_b32 s6, s13, 11
	s_or_b32 s6, s6, s14
	v_or_b32_e32 v4, s6, v134
	v_mul_hi_i32_i24_e32 v5, 0x1c00, v4
	v_mul_i32_i24_e32 v4, 0x1c00, v4
	v_lshl_add_u64 v[4:5], s[8:9], 0, v[4:5]
	s_mov_b32 s27, s7
	v_readlane_b32 s37, v250, 33
	v_readlane_b32 s38, v250, 34
	v_readlane_b32 s39, v250, 35
	v_readlane_b32 s40, v250, 36
	v_readlane_b32 s41, v250, 37
	v_lshl_add_u64 v[130:131], v[4:5], 0, s[26:27]
	s_mov_b64 s[14:15], 0

.LBB0_1603:
	s_or_b64 exec, exec, s[2:3]
	s_abs_i32 s29, s28
	v_cvt_f32_u32_e32 v1, s29
	s_add_i32 s2, s28, 0x2fff
	s_sub_i32 s5, 0, s29
	s_xor_b32 s3, s2, s28
	v_rcp_iflag_f32_e32 v1, v1
	s_ashr_i32 s4, s3, 31
	s_abs_i32 s2, s2
	s_mov_b32 s25, 0
	v_mul_f32_e32 v1, 0x4f7ffffe, v1
	v_cvt_u32_f32_e32 v1, v1
	s_waitcnt lgkmcnt(0)
	s_barrier
	v_readfirstlane_b32 s30, v1
	s_mul_i32 s5, s5, s30
	s_mul_hi_u32 s3, s30, s5
	s_add_i32 s30, s30, s3
	s_mul_hi_u32 s3, s2, s30
	s_mul_i32 s5, s3, s29
	s_sub_i32 s2, s2, s5
	s_add_i32 s6, s3, 1
	s_sub_i32 s5, s2, s29
	s_cmp_ge_u32 s2, s29
	s_cselect_b32 s3, s6, s3
	s_cselect_b32 s2, s5, s2
	s_add_i32 s5, s3, 1
	s_cmp_ge_u32 s2, s29
	s_cselect_b32 s2, s5, s3
	s_xor_b32 s5, s2, s4
	v_readlane_b32 s2, v250, 53
	s_cmpk_lt_i32 s2, 0x2000
	v_readlane_b32 s3, v250, 54
	s_cbranch_scc1 .LBB0_1605
	v_mov_b32_e32 v183, 0
	v_readlane_b32 s2, v250, 55
	v_and_b32_e32 v98, 0x70, v198
	s_xor_b32 s33, s2, 0x80000000
	v_mov_b32_e32 v99, v183
	s_sub_i32 s31, s5, s4
	s_cbranch_execz .LBB0_1606
	s_branch .LBB0_1635

.LBB0_1610:
	s_abs_i32 s3, s8
	s_mul_hi_u32 s4, s3, s30
	s_mul_i32 s4, s4, s29
	s_sub_i32 s3, s3, s4
	s_ashr_i32 s2, s8, 31
	s_sub_i32 s4, s3, s29
	s_cmp_ge_u32 s3, s29
	s_cselect_b32 s3, s4, s3
	s_sub_i32 s4, s3, s29
	s_cmp_ge_u32 s3, s29
	s_cselect_b32 s3, s4, s3
	s_xor_b32 s3, s3, s2
	s_sub_i32 s4, s3, s2
	s_add_i32 s48, s7, s4
	s_cmp_gt_i32 s48, 0x2fff
	s_cselect_b64 s[2:3], -1, 0
	s_and_b64 vcc, exec, s[2:3]
	s_cbranch_vccnz .LBB0_1612
	s_lshl_b32 s2, s4, 2
	s_add_i32 s2, s2, 0
	s_add_i32 s2, s2, 0x20400
	v_mov_b32_e32 v100, s2
	ds_read_b32 v100, v100
	s_waitcnt lgkmcnt(0)
	v_cmp_lt_i32_e64 s[2:3], s48, v100

.LBB0_1641:
	s_abs_i32 s7, s17
	s_mul_hi_u32 s8, s7, s30
	s_mul_i32 s8, s8, s29
	s_sub_i32 s7, s7, s8
	s_ashr_i32 s6, s17, 31
	s_sub_i32 s8, s7, s29
	s_cmp_ge_u32 s7, s29
	s_cselect_b32 s7, s8, s7
	s_sub_i32 s8, s7, s29
	s_cmp_ge_u32 s7, s29
	s_cselect_b32 s7, s8, s7
	s_xor_b32 s7, s7, s6
	s_sub_i32 s6, s7, s6
	s_add_i32 s16, s4, s6
	s_cmp_gt_i32 s16, 0x2fff
	s_cselect_b64 s[8:9], -1, 0
	s_and_b64 vcc, exec, s[8:9]
	s_cbranch_vccnz .LBB0_1643
	s_lshl_b32 s6, s6, 2
	s_add_i32 s6, s6, 0
	s_add_i32 s6, s6, 0x20400
	v_mov_b32_e32 v2, s6
	ds_read_b32 v2, v2
	s_waitcnt lgkmcnt(0)
	v_cmp_lt_i32_e64 s[8:9], s16, v2

	.amdhsa_kernel _Z8yoco_fwd4Args
		.amdhsa_group_segment_fixed_size 0
		.amdhsa_private_segment_fixed_size 0
		.amdhsa_kernarg_size 504
		.amdhsa_user_sgpr_count 2
		.amdhsa_user_sgpr_dispatch_ptr 0
		.amdhsa_user_sgpr_queue_ptr 0
		.amdhsa_user_sgpr_kernarg_segment_ptr 1
		.amdhsa_user_sgpr_dispatch_id 0
		.amdhsa_user_sgpr_kernarg_preload_length 0
		.amdhsa_user_sgpr_kernarg_preload_offset 0
		.amdhsa_user_sgpr_private_segment_size 0
		.amdhsa_uses_dynamic_stack 0
		.amdhsa_enable_private_segment 0
		.amdhsa_system_sgpr_workgroup_id_x 1
		.amdhsa_system_sgpr_workgroup_id_y 0
		.amdhsa_system_sgpr_workgroup_id_z 0
		.amdhsa_system_sgpr_workgroup_info 0
		.amdhsa_system_vgpr_workitem_id 0
		.amdhsa_next_free_vgpr 256
		.amdhsa_next_free_sgpr 99
		.amdhsa_accum_offset 256
		.amdhsa_reserve_vcc 1
		.amdhsa_float_round_mode_32 0
		.amdhsa_float_round_mode_16_64 0
		.amdhsa_float_denorm_mode_32 3
		.amdhsa_float_denorm_mode_16_64 3
		.amdhsa_dx10_clamp 1
		.amdhsa_ieee_mode 1
		.amdhsa_fp16_overflow 0
		.amdhsa_tg_split 0
		.amdhsa_exception_fp_ieee_invalid_op 0
		.amdhsa_exception_fp_denorm_src 0
		.amdhsa_exception_fp_ieee_div_zero 0
		.amdhsa_exception_fp_ieee_overflow 0
		.amdhsa_exception_fp_ieee_underflow 0
		.amdhsa_exception_fp_ieee_inexact 0
		.amdhsa_exception_int_div_zero 0
	.end_amdhsa_kernel

amdhsa.kernels:
  - .agpr_count:     0
    .args:
      - .offset:         0
        .size:           248
        .value_kind:     by_value
      - .offset:         248
        .size:           4
        .value_kind:     hidden_block_count_x
      - .offset:         252
        .size:           4
        .value_kind:     hidden_block_count_y
      - .offset:         256
        .size:           4
        .value_kind:     hidden_block_count_z
      - .offset:         260
        .size:           2
        .value_kind:     hidden_group_size_x
      - .offset:         262
        .size:           2
        .value_kind:     hidden_group_size_y
      - .offset:         264
        .size:           2
        .value_kind:     hidden_group_size_z
      - .offset:         266
        .size:           2
        .value_kind:     hidden_remainder_x
      - .offset:         268
        .size:           2
        .value_kind:     hidden_remainder_y
      - .offset:         270
        .size:           2
        .value_kind:     hidden_remainder_z
      - .offset:         288
        .size:           8
        .value_kind:     hidden_global_offset_x
      - .offset:         296
        .size:           8
        .value_kind:     hidden_global_offset_y
      - .offset:         304
        .size:           8
        .value_kind:     hidden_global_offset_z
      - .offset:         312
        .size:           2
        .value_kind:     hidden_grid_dims
      - .offset:         368
        .size:           4
        .value_kind:     hidden_dynamic_lds_size
    .group_segment_fixed_size: 0
    .kernarg_segment_align: 8
    .kernarg_segment_size: 504
    .language:       OpenCL C
    .language_version:
      - 2
      - 0
    .max_flat_workgroup_size: 512
    .name:           _Z8yoco_fwd4Args
    .private_segment_fixed_size: 0
    .sgpr_count:     105
    .sgpr_spill_count: 440
    .symbol:         _Z8yoco_fwd4Args.kd
    .uniform_work_group_size: 1
    .uses_dynamic_stack: false
    .vgpr_count:     256
    .vgpr_spill_count: 0
    .wavefront_size: 64
